# v3 + scan-output MFMA-first waves load next-chunk operands at segment start + fp8 MFMAs issued in the 8-byte unscaled f8f6f4 encoding (unit scales)
# baseline (speedup 1.0000x reference)
.LBB0_415:
	v_mov_b32_e32 v212, v15
	s_and_b32 s0, s74, 1
	v_ashrrev_i32_e32 v213, 31, v212
	v_lshlrev_b64 v[2:3], 11, v[212:213]
	v_lshl_add_u64 v[2:3], s[22:23], 0, v[2:3]
	v_lshl_add_u64 v[208:209], v[206:207], 0, v[2:3]
	v_add_co_u32_e32 v2, vcc, 0x2e200000, v208
	v_lshl_add_u64 v[210:211], v[208:209], 0, s[12:13]
	s_nop 0
	v_addc_co_u32_e32 v3, vcc, 0, v209, vcc
	global_load_dwordx4 v[6:9], v[2:3], off
	s_nop 0
	global_load_dwordx4 v[2:5], v[210:211], off offset:16
	s_mul_i32 s1, s0, 0x11a00
	s_xor_b32 s0, s0, 1
	s_mul_i32 s0, s0, 0x11a00
	s_add_i32 s76, s1, 0
	s_add_i32 s78, s0, 0
	s_mov_b64 s[0:1], -1
	s_and_b64 vcc, exec, s[6:7]
	s_cbranch_vccz .LBB0_429
	s_cmp_gt_u32 s74, 6
	s_cbranch_scc1 .Lp4a_noload
	v_lshlrev_b32_e32 v180, 4, v214
	v_and_b32_e32 v182, 3, v214
	v_and_b32_e32 v184, 0xffffffc0, v180
	v_mov_b32_e32 v185, 0
	v_lshlrev_b32_e32 v184, 1, v184
	s_add_u32 s98, s75, s22
	v_lshl_or_b32 v184, v182, 5, v184
	s_addc_u32 s99, s77, s23
	v_mov_b32_e32 v181, 0
	v_lshl_add_u64 v[184:185], s[98:99], 0, v[184:185]
	v_lshl_add_u64 v[180:181], s[98:99], 0, v[180:181]
	s_mov_b64 s[100:101], 0x1e220000
	v_lshl_add_u64 v[186:187], v[184:185], 0, s[100:101]
	s_mov_b64 s[100:101], 0x16220000
	v_lshl_add_u64 v[188:189], v[184:185], 0, s[100:101]
	s_mov_b64 s[100:101], 0x26220000
	v_lshl_add_u64 v[190:191], v[180:181], 0, s[100:101]
	s_mov_b64 s[100:101], 0x26222000
	v_lshl_add_u64 v[180:181], v[180:181], 0, s[100:101]
	global_load_dwordx4 v[160:163], v[186:187], off
	global_load_dwordx4 v[10:13], v[186:187], off offset:16
	global_load_dwordx4 v[164:167], v[188:189], off
	global_load_dwordx4 v[168:171], v[188:189], off offset:16
	global_load_dwordx4 v[172:175], v[190:191], off
	global_load_dwordx4 v[176:179], v[180:181], off
.Lp4a_noload:
	v_mov_b32_e32 v0, v214
	v_mov_b32_e32 v80, s76
	v_and_b32_e32 v188, 31, v0
	v_bfe_u32 v189, v0, 5, 1
	v_or_b32_e32 v0, s37, v188
	v_mad_u32_u24 v139, v0, s64, v80
	v_lshlrev_b32_e32 v137, 4, v189
	v_add_u32_e32 v80, v139, v137
	ds_read_b128 v[124:127], v80
	ds_read_b128 v[120:123], v80 offset:32
	ds_read_b128 v[116:119], v80 offset:64
	ds_read_b128 v[112:115], v80 offset:96
	ds_read_b128 v[108:111], v80 offset:128
	ds_read_b128 v[104:107], v80 offset:160
	ds_read_b128 v[100:103], v80 offset:192
	ds_read_b128 v[96:99], v80 offset:224
	v_or_b32_e32 v80, s8, v188
	v_mul_lo_u32 v80, v80, s60
	v_add_u32_e32 v138, s76, v80
	v_lshlrev_b32_e32 v190, 3, v189
	v_add_u32_e32 v136, s76, v137
	v_add_u32_e32 v128, v138, v190
	s_and_b64 vcc, exec, s[10:11]
	s_cbranch_vccz .LBB0_442
	v_mad_u32_u24 v84, v188, s64, v136
	ds_read_b128 v[80:83], v84 offset:17408
	ds_read_b128 v[130:133], v84 offset:17440
	ds_read_b128 v[140:143], v84 offset:17472
	ds_read_b128 v[144:147], v84 offset:17504
	ds_read_b128 v[148:151], v84 offset:17536
	ds_read_b128 v[152:155], v84 offset:17568
	ds_read_b128 v[156:159], v84 offset:17600
	ds_read_b128 v[180:183], v84 offset:17632
	v_add_u32_e32 v84, 0xd000, v128
	ds_read2_b64 v[184:187], v84 offset1:2
	ds_read2_b64 v[192:195], v84 offset0:4 offset1:6
	s_waitcnt lgkmcnt(0)
	s_waitcnt lgkmcnt(9)
	v_mfma_f32_32x32x16_bf16 v[80:95], v[80:83], v[124:127], 0
	s_waitcnt lgkmcnt(8)
	v_mfma_f32_32x32x16_bf16 v[80:95], v[130:133], v[120:123], v[80:95]
	s_waitcnt lgkmcnt(7)
	v_mfma_f32_32x32x16_bf16 v[80:95], v[140:143], v[116:119], v[80:95]
	s_waitcnt lgkmcnt(6)
	v_mfma_f32_32x32x16_bf16 v[80:95], v[144:147], v[112:115], v[80:95]
	s_waitcnt lgkmcnt(5)
	v_mfma_f32_32x32x16_bf16 v[80:95], v[148:151], v[108:111], v[80:95]
	s_waitcnt lgkmcnt(4)
	v_mfma_f32_32x32x16_bf16 v[80:95], v[152:155], v[104:107], v[80:95]
	s_waitcnt lgkmcnt(3)
	v_mfma_f32_32x32x16_bf16 v[80:95], v[156:159], v[100:103], v[80:95]
	s_waitcnt lgkmcnt(2)
	v_mfma_f32_32x32x16_bf16 v[80:95], v[180:183], v[96:99], v[80:95]
	s_nop 11
	v_cvt_pk_bf16_f32 v80, v80, v81
	v_cvt_pk_bf16_f32 v81, v82, v83
	v_cvt_pk_bf16_f32 v82, v84, v85
	v_cvt_pk_bf16_f32 v83, v86, v87
	s_waitcnt lgkmcnt(1)
	s_nop 0
	v_mfma_f32_32x32x16_bf16 v[144:159], v[184:187], v[80:83], 0
	v_cvt_pk_bf16_f32 v80, v88, v89
	v_cvt_pk_bf16_f32 v81, v90, v91
	v_cvt_pk_bf16_f32 v82, v92, v93
	v_cvt_pk_bf16_f32 v83, v94, v95
	s_waitcnt lgkmcnt(0)
	s_nop 0
	v_mfma_f32_32x32x16_bf16 v[144:159], v[192:195], v[80:83], v[144:159]
	s_mov_b32 s0, 1
	s_cbranch_execnz .LBB0_419

.LBB0_423:
	s_or_b64 exec, exec, s[0:1]
	v_mul_u32_u24_e32 v0, 0x110, v0
	v_add3_u32 v0, s39, v0, v190
	v_cvt_pk_bf16_f32 v144, v144, v145
	v_cvt_pk_bf16_f32 v145, v146, v147
	v_cvt_pk_bf16_f32 v146, v148, v149
	v_cvt_pk_bf16_f32 v147, v150, v151
	s_waitcnt vmcnt(0)
	v_mov_b64_e32 v[198:199], v[178:179]
	v_mov_b64_e32 v[202:203], v[174:175]
	v_mov_b64_e32 v[186:187], v[170:171]
	v_mov_b64_e32 v[194:195], v[166:167]
	s_waitcnt lgkmcnt(0)
	v_mov_b64_e32 v[182:183], v[162:163]
	v_mov_b64_e32 v[190:191], v[12:13]
	ds_write2_b64 v0, v[144:145], v[146:147] offset1:2
	v_cvt_pk_bf16_f32 v144, v152, v153
	v_cvt_pk_bf16_f32 v145, v154, v155
	v_cvt_pk_bf16_f32 v146, v156, v157
	v_cvt_pk_bf16_f32 v147, v158, v159
	s_cmp_eq_u32 s22, 0xe0000
	v_mov_b64_e32 v[196:197], v[176:177]
	v_mov_b64_e32 v[200:201], v[172:173]
	v_mov_b64_e32 v[184:185], v[168:169]
	v_mov_b64_e32 v[192:193], v[164:165]
	v_mov_b64_e32 v[180:181], v[160:161]
	v_mov_b64_e32 v[188:189], v[10:11]
	ds_write2_b64 v0, v[144:145], v[146:147] offset0:4 offset1:6
	s_cbranch_scc1 .LBB0_428
	v_cvt_f32_f16_e32 v144, v160
	v_cvt_f32_f16_sdwa v145, v160 dst_sel:DWORD dst_unused:UNUSED_PAD src0_sel:WORD_1
	v_cvt_f32_f16_e32 v150, v161
	v_cvt_f32_f16_sdwa v151, v161 dst_sel:DWORD dst_unused:UNUSED_PAD src0_sel:WORD_1
	v_cvt_f32_f16_e32 v155, v162
	v_add_f32_e32 v192, 0, v144
	v_cvt_f32_f16_sdwa v156, v162 dst_sel:DWORD dst_unused:UNUSED_PAD src0_sel:WORD_1
	v_add_f32_e32 v193, v192, v145
	v_cvt_f32_f16_e32 v159, v163
	v_add_f32_e32 v194, v193, v150
	v_cvt_f32_f16_sdwa v180, v163 dst_sel:DWORD dst_unused:UNUSED_PAD src0_sel:WORD_1
	v_add_f32_e32 v195, v194, v151
	v_cvt_f32_f16_e32 v183, v10
	v_add_f32_e32 v196, v195, v155
	v_cvt_f32_f16_sdwa v184, v10 dst_sel:DWORD dst_unused:UNUSED_PAD src0_sel:WORD_1
	v_add_f32_e32 v197, v196, v156
	v_cvt_f32_f16_e32 v186, v11
	v_add_f32_e32 v198, v197, v159
	v_cvt_f32_f16_sdwa v187, v11 dst_sel:DWORD dst_unused:UNUSED_PAD src0_sel:WORD_1
	v_add_f32_e32 v199, v198, v180
	v_cvt_f32_f16_e32 v188, v12
	v_add_f32_e32 v200, v199, v183
	v_cvt_f32_f16_sdwa v189, v12 dst_sel:DWORD dst_unused:UNUSED_PAD src0_sel:WORD_1
	v_add_f32_e32 v201, v200, v184
	v_cvt_f32_f16_e32 v190, v13
	v_add_f32_e32 v202, v201, v186
	v_cvt_f32_f16_sdwa v191, v13 dst_sel:DWORD dst_unused:UNUSED_PAD src0_sel:WORD_1
	v_add_f32_e32 v203, v202, v187
	v_add_f32_e32 v213, v203, v188
	v_add_f32_e32 v220, v213, v189
	v_add_f32_e32 v221, v220, v190
	v_add_f32_e32 v222, v221, v191
	ds_bpermute_b32 v149, v215, v222
	v_mov_b32_e32 v148, v214
	v_mul_f32_e32 v144, 0x3fb8aa3b, v144
	v_and_b32_e32 v0, 3, v148
	s_waitcnt lgkmcnt(0)
	v_add_f32_e32 v149, v222, v149
	v_cmp_eq_u32_e32 vcc, 0, v0
	v_cmp_lt_u32_e64 s[2:3], 1, v0
	v_exp_f32_e32 v144, v144
	v_cndmask_b32_e32 v149, v149, v222, vcc
	ds_bpermute_b32 v226, v216, v149
	v_lshlrev_b32_e32 v146, 16, v164
	v_sub_f32_e32 v144, 1.0, v144
	v_mul_f32_e32 v145, 0x3fb8aa3b, v145
	v_exp_f32_e32 v145, v145
	s_waitcnt lgkmcnt(0)
	v_add_f32_e32 v226, v149, v226
	v_cndmask_b32_e64 v226, v149, v226, s[2:3]
	ds_bpermute_b32 v149, v217, v226
	v_sub_f32_e32 v226, v226, v222
	v_add_f32_e32 v192, v192, v226
	v_mul_f32_e32 v232, 0x3fb8aa3b, v192
	v_max_f32_e32 v233, 0xc2a00000, v192
	s_waitcnt lgkmcnt(0)
	v_sub_f32_e32 v192, v149, v192
	v_mul_f32_e32 v233, 0xbfb8aa3b, v233
	v_mul_f32_e32 v192, 0x3fb8aa3b, v192
	v_exp_f32_e32 v232, v232
	v_exp_f32_e32 v233, v233
	v_exp_f32_e32 v192, v192
	v_ashrrev_i32_e32 v154, 2, v148
	v_mul_f32_e32 v146, v232, v146
	v_mul_f32_e32 v232, v144, v233
	v_mul_f32_e32 v144, v144, v192
	v_add_f32_e32 v192, v193, v226
	v_mul_f32_e32 v193, 0x3fb8aa3b, v192
	v_max_f32_e32 v233, 0xc2a00000, v192
	v_sub_f32_e32 v192, v149, v192
	v_mul_f32_e32 v233, 0xbfb8aa3b, v233
	v_mul_f32_e32 v192, 0x3fb8aa3b, v192
	v_exp_f32_e32 v193, v193
	v_exp_f32_e32 v233, v233
	v_exp_f32_e32 v192, v192
	v_and_b32_e32 v147, 0xffff0000, v164
	v_sub_f32_e32 v145, 1.0, v145
	v_lshlrev_b32_e32 v231, 1, v154
	v_mul_f32_e32 v147, v193, v147
	v_mul_f32_e32 v193, v145, v233
	v_mul_f32_e32 v145, v145, v192
	v_mul_u32_u24_e32 v192, 0x1100, v0
	v_cvt_pk_bf16_f32 v146, v146, v147
	v_add3_u32 v192, s78, v231, v192
	v_cvt_pk_bf16_f32 v147, v232, v193
	ds_write_b16 v192, v146
	ds_write_b16_d16_hi v192, v146 offset:272
	ds_write_b16 v192, v147 offset:17408
	ds_write_b16_d16_hi v192, v147 offset:17680
	v_cvt_pk_bf16_f32 v144, v144, v145
	v_add_f32_e32 v145, v194, v226
	v_mul_f32_e32 v146, 0x3fb8aa3b, v150
	v_mul_f32_e32 v147, 0x3fb8aa3b, v145
	v_max_f32_e32 v150, 0xc2a00000, v145
	v_sub_f32_e32 v145, v149, v145
	v_exp_f32_e32 v146, v146
	v_mul_f32_e32 v150, 0xbfb8aa3b, v150
	v_mul_f32_e32 v145, 0x3fb8aa3b, v145
	v_exp_f32_e32 v150, v150
	v_exp_f32_e32 v145, v145
	v_exp_f32_e32 v147, v147
	v_sub_f32_e32 v146, 1.0, v146
	v_lshlrev_b32_e32 v152, 16, v165
	v_mul_f32_e32 v150, v146, v150
	v_mul_f32_e32 v145, v146, v145
	v_add_f32_e32 v146, v195, v226
	v_mul_f32_e32 v147, v147, v152
	v_mul_f32_e32 v151, 0x3fb8aa3b, v151
	v_mul_f32_e32 v152, 0x3fb8aa3b, v146
	v_max_f32_e32 v193, 0xc2a00000, v146
	v_sub_f32_e32 v146, v149, v146
	v_exp_f32_e32 v151, v151
	v_mul_f32_e32 v146, 0x3fb8aa3b, v146
	v_exp_f32_e32 v152, v152
	v_mul_f32_e32 v193, 0xbfb8aa3b, v193
	v_exp_f32_e32 v146, v146
	v_exp_f32_e32 v193, v193
	v_and_b32_e32 v153, 0xffff0000, v165
	v_sub_f32_e32 v151, 1.0, v151
	v_mul_f32_e32 v152, v152, v153
	v_mul_f32_e32 v146, v151, v146
	v_cvt_pk_bf16_f32 v147, v147, v152
	v_mul_f32_e32 v153, v151, v193
	v_cvt_pk_bf16_f32 v150, v150, v153
	ds_write_b16 v192, v147 offset:544
	ds_write_b16_d16_hi v192, v147 offset:816
	ds_write_b16 v192, v150 offset:17952
	ds_write_b16_d16_hi v192, v150 offset:18224
	v_cvt_pk_bf16_f32 v145, v145, v146
	v_add_f32_e32 v146, v196, v226
	v_mul_f32_e32 v147, 0x3fb8aa3b, v155
	v_mul_f32_e32 v150, 0x3fb8aa3b, v146
	v_max_f32_e32 v151, 0xc2a00000, v146
	v_sub_f32_e32 v146, v149, v146
	v_exp_f32_e32 v147, v147
	v_mul_f32_e32 v151, 0xbfb8aa3b, v151
	v_mul_f32_e32 v146, 0x3fb8aa3b, v146
	v_exp_f32_e32 v151, v151
	v_exp_f32_e32 v146, v146
	v_sub_f32_e32 v147, 1.0, v147
	v_mul_f32_e32 v152, 0x3fb8aa3b, v156
	v_mul_f32_e32 v151, v147, v151
	v_mul_f32_e32 v146, v147, v146
	v_add_f32_e32 v147, v197, v226
	v_mul_f32_e32 v153, 0x3fb8aa3b, v147
	v_max_f32_e32 v155, 0xc2a00000, v147
	v_sub_f32_e32 v147, v149, v147
	v_exp_f32_e32 v150, v150
	v_exp_f32_e32 v152, v152
	v_mul_f32_e32 v147, 0x3fb8aa3b, v147
	v_exp_f32_e32 v153, v153
	v_mul_f32_e32 v155, 0xbfb8aa3b, v155
	v_exp_f32_e32 v147, v147
	v_exp_f32_e32 v155, v155
	v_lshlrev_b32_e32 v157, 16, v166
	v_and_b32_e32 v158, 0xffff0000, v166
	v_mul_f32_e32 v150, v150, v157
	v_sub_f32_e32 v152, 1.0, v152
	v_mul_f32_e32 v153, v153, v158
	v_mul_f32_e32 v147, v152, v147
	v_cvt_pk_bf16_f32 v150, v150, v153
	v_mul_f32_e32 v155, v152, v155
	v_cvt_pk_bf16_f32 v151, v151, v155
	ds_write_b16 v192, v150 offset:1088
	ds_write_b16_d16_hi v192, v150 offset:1360
	ds_write_b16 v192, v151 offset:18496
	ds_write_b16_d16_hi v192, v151 offset:18768
	v_cvt_pk_bf16_f32 v146, v146, v147
	v_add_f32_e32 v147, v198, v226
	v_mul_f32_e32 v150, 0x3fb8aa3b, v159
	v_mul_f32_e32 v151, 0x3fb8aa3b, v147
	v_max_f32_e32 v152, 0xc2a00000, v147
	v_sub_f32_e32 v147, v149, v147
	v_exp_f32_e32 v150, v150
	v_mul_f32_e32 v152, 0xbfb8aa3b, v152
	v_mul_f32_e32 v147, 0x3fb8aa3b, v147
	v_exp_f32_e32 v152, v152
	v_exp_f32_e32 v147, v147
	v_sub_f32_e32 v150, 1.0, v150
	v_mul_f32_e32 v153, 0x3fb8aa3b, v180
	v_mul_f32_e32 v152, v150, v152
	v_mul_f32_e32 v147, v150, v147
	v_add_f32_e32 v150, v199, v226
	v_mul_f32_e32 v155, 0x3fb8aa3b, v150
	v_max_f32_e32 v156, 0xc2a00000, v150
	v_sub_f32_e32 v150, v149, v150
	v_exp_f32_e32 v151, v151
	v_exp_f32_e32 v153, v153
	v_mul_f32_e32 v150, 0x3fb8aa3b, v150
	v_exp_f32_e32 v155, v155
	v_mul_f32_e32 v156, 0xbfb8aa3b, v156
	v_exp_f32_e32 v150, v150
	v_exp_f32_e32 v156, v156
	v_lshlrev_b32_e32 v181, 16, v167
	v_and_b32_e32 v182, 0xffff0000, v167
	v_mul_f32_e32 v151, v151, v181
	v_sub_f32_e32 v153, 1.0, v153
	v_mul_f32_e32 v155, v155, v182
	v_mul_f32_e32 v150, v153, v150
	v_cvt_pk_bf16_f32 v151, v151, v155
	v_mul_f32_e32 v156, v153, v156
	v_cvt_pk_bf16_f32 v152, v152, v156
	ds_write_b16 v192, v151 offset:1632
	ds_write_b16_d16_hi v192, v151 offset:1904
	ds_write_b16 v192, v152 offset:19040
	ds_write_b16_d16_hi v192, v152 offset:19312
	v_cvt_pk_bf16_f32 v147, v147, v150
	v_add_f32_e32 v150, v200, v226
	v_mul_f32_e32 v151, 0x3fb8aa3b, v183
	v_mul_f32_e32 v152, 0x3fb8aa3b, v150
	v_max_f32_e32 v153, 0xc2a00000, v150
	v_sub_f32_e32 v150, v149, v150
	v_exp_f32_e32 v151, v151
	v_mul_f32_e32 v153, 0xbfb8aa3b, v153
	v_mul_f32_e32 v150, 0x3fb8aa3b, v150
	v_exp_f32_e32 v153, v153
	v_exp_f32_e32 v150, v150
	v_sub_f32_e32 v151, 1.0, v151
	v_mul_f32_e32 v155, 0x3fb8aa3b, v184
	v_mul_f32_e32 v153, v151, v153
	v_mul_f32_e32 v150, v151, v150
	v_add_f32_e32 v151, v201, v226
	v_mul_f32_e32 v156, 0x3fb8aa3b, v151
	v_max_f32_e32 v157, 0xc2a00000, v151
	v_sub_f32_e32 v151, v149, v151
	v_exp_f32_e32 v152, v152
	v_exp_f32_e32 v155, v155
	v_mul_f32_e32 v151, 0x3fb8aa3b, v151
	v_exp_f32_e32 v156, v156
	v_mul_f32_e32 v157, 0xbfb8aa3b, v157
	v_exp_f32_e32 v151, v151
	v_exp_f32_e32 v157, v157
	v_lshlrev_b32_e32 v185, 16, v168
	v_and_b32_e32 v223, 0xffff0000, v168
	v_mul_f32_e32 v152, v152, v185
	v_sub_f32_e32 v155, 1.0, v155
	v_mul_f32_e32 v156, v156, v223
	v_mul_f32_e32 v151, v155, v151
	v_cvt_pk_bf16_f32 v152, v152, v156
	v_mul_f32_e32 v157, v155, v157
	v_cvt_pk_bf16_f32 v153, v153, v157
	ds_write_b16 v192, v152 offset:2176
	ds_write_b16_d16_hi v192, v152 offset:2448
	ds_write_b16 v192, v153 offset:19584
	ds_write_b16_d16_hi v192, v153 offset:19856
	v_cvt_pk_bf16_f32 v150, v150, v151
	v_add_f32_e32 v151, v202, v226
	v_mul_f32_e32 v152, 0x3fb8aa3b, v186
	v_mul_f32_e32 v153, 0x3fb8aa3b, v151
	v_max_f32_e32 v155, 0xc2a00000, v151
	v_sub_f32_e32 v151, v149, v151
	v_exp_f32_e32 v152, v152
	v_mul_f32_e32 v155, 0xbfb8aa3b, v155
	v_mul_f32_e32 v151, 0x3fb8aa3b, v151
	v_exp_f32_e32 v155, v155
	v_exp_f32_e32 v151, v151
	v_sub_f32_e32 v152, 1.0, v152
	v_mul_f32_e32 v156, 0x3fb8aa3b, v187
	v_mul_f32_e32 v155, v152, v155
	v_mul_f32_e32 v151, v152, v151
	v_add_f32_e32 v152, v203, v226
	v_mul_f32_e32 v157, 0x3fb8aa3b, v152
	v_max_f32_e32 v158, 0xc2a00000, v152
	v_sub_f32_e32 v152, v149, v152
	v_exp_f32_e32 v153, v153
	v_exp_f32_e32 v156, v156
	v_mul_f32_e32 v152, 0x3fb8aa3b, v152
	v_exp_f32_e32 v157, v157
	v_mul_f32_e32 v158, 0xbfb8aa3b, v158
	v_exp_f32_e32 v152, v152
	v_exp_f32_e32 v158, v158
	v_lshlrev_b32_e32 v224, 16, v169
	v_and_b32_e32 v225, 0xffff0000, v169
	v_mul_f32_e32 v153, v153, v224
	v_sub_f32_e32 v156, 1.0, v156
	v_mul_f32_e32 v157, v157, v225
	v_mul_f32_e32 v152, v156, v152
	v_cvt_pk_bf16_f32 v153, v153, v157
	v_mul_f32_e32 v158, v156, v158
	v_cvt_pk_bf16_f32 v155, v155, v158
	ds_write_b16 v192, v153 offset:2720
	ds_write_b16_d16_hi v192, v153 offset:2992
	ds_write_b16 v192, v155 offset:20128
	ds_write_b16_d16_hi v192, v155 offset:20400
	v_cvt_pk_bf16_f32 v151, v151, v152
	v_add_f32_e32 v152, v213, v226
	v_mul_f32_e32 v153, 0x3fb8aa3b, v188
	v_mul_f32_e32 v155, 0x3fb8aa3b, v152
	v_max_f32_e32 v156, 0xc2a00000, v152
	v_sub_f32_e32 v152, v149, v152
	v_exp_f32_e32 v153, v153
	v_mul_f32_e32 v156, 0xbfb8aa3b, v156
	v_mul_f32_e32 v152, 0x3fb8aa3b, v152
	v_exp_f32_e32 v156, v156
	v_exp_f32_e32 v152, v152
	v_sub_f32_e32 v153, 1.0, v153
	v_mul_f32_e32 v157, 0x3fb8aa3b, v189
	v_mul_f32_e32 v156, v153, v156
	v_mul_f32_e32 v152, v153, v152
	v_add_f32_e32 v153, v220, v226
	v_mul_f32_e32 v158, 0x3fb8aa3b, v153
	v_max_f32_e32 v159, 0xc2a00000, v153
	v_sub_f32_e32 v153, v149, v153
	v_exp_f32_e32 v155, v155
	v_exp_f32_e32 v157, v157
	v_mul_f32_e32 v153, 0x3fb8aa3b, v153
	v_exp_f32_e32 v158, v158
	v_mul_f32_e32 v159, 0xbfb8aa3b, v159
	v_exp_f32_e32 v153, v153
	v_exp_f32_e32 v159, v159
	v_lshlrev_b32_e32 v227, 16, v170
	v_and_b32_e32 v228, 0xffff0000, v170
	v_mul_f32_e32 v155, v155, v227
	v_sub_f32_e32 v157, 1.0, v157
	v_mul_f32_e32 v158, v158, v228
	v_mul_f32_e32 v153, v157, v153
	v_cvt_pk_bf16_f32 v155, v155, v158
	v_mul_f32_e32 v159, v157, v159
	v_cvt_pk_bf16_f32 v156, v156, v159
	ds_write_b16 v192, v155 offset:3264
	ds_write_b16_d16_hi v192, v155 offset:3536
	ds_write_b16 v192, v156 offset:20672
	ds_write_b16_d16_hi v192, v156 offset:20944
	v_cvt_pk_bf16_f32 v152, v152, v153
	v_add_f32_e32 v153, v221, v226
	v_mul_f32_e32 v155, 0x3fb8aa3b, v190
	v_mul_f32_e32 v156, 0x3fb8aa3b, v153
	v_max_f32_e32 v157, 0xc2a00000, v153
	v_sub_f32_e32 v153, v149, v153
	v_exp_f32_e32 v155, v155
	v_mul_f32_e32 v157, 0xbfb8aa3b, v157
	v_mul_f32_e32 v153, 0x3fb8aa3b, v153
	v_exp_f32_e32 v157, v157
	v_exp_f32_e32 v153, v153
	v_sub_f32_e32 v155, 1.0, v155
	v_mul_f32_e32 v158, 0x3fb8aa3b, v191
	v_mul_f32_e32 v157, v155, v157
	v_mul_f32_e32 v153, v155, v153
	v_add_f32_e32 v155, v222, v226
	v_mul_f32_e32 v159, 0x3fb8aa3b, v155
	v_max_f32_e32 v180, 0xc2a00000, v155
	v_sub_f32_e32 v155, v149, v155
	v_exp_f32_e32 v156, v156
	v_exp_f32_e32 v158, v158
	v_mul_f32_e32 v155, 0x3fb8aa3b, v155
	v_exp_f32_e32 v159, v159
	v_mul_f32_e32 v180, 0xbfb8aa3b, v180
	v_exp_f32_e32 v155, v155
	v_exp_f32_e32 v180, v180
	v_lshlrev_b32_e32 v229, 16, v171
	v_and_b32_e32 v230, 0xffff0000, v171
	v_mul_f32_e32 v156, v156, v229
	v_sub_f32_e32 v158, 1.0, v158
	v_mul_f32_e32 v159, v159, v230
	v_mul_f32_e32 v155, v158, v155
	v_cvt_pk_bf16_f32 v156, v156, v159
	v_mul_f32_e32 v180, v158, v180
	v_cvt_pk_bf16_f32 v157, v157, v180
	ds_write_b16 v192, v156 offset:3808
	ds_write_b16_d16_hi v192, v156 offset:4080
	ds_write_b16 v192, v157 offset:21216
	ds_write_b16_d16_hi v192, v157 offset:21488
	v_cvt_pk_bf16_f32 v153, v153, v155
	v_mul_lo_u32 v154, v154, s60
	v_lshlrev_b32_e32 v155, 5, v0
	v_add3_u32 v154, s78, v154, v155
	ds_write_b128 v154, v[144:147] offset:34816
	ds_write_b128 v154, v[150:153] offset:34832
	s_and_saveexec_b64 s[0:1], vcc
	s_cbranch_execz .LBB0_426
	v_mul_f32_e32 v144, 0x3fb8aa3b, v149
	v_exp_f32_e32 v144, v144
	v_add_u32_e32 v145, s78, v148
	v_add_u32_e32 v145, 0x11800, v145
	ds_write_b32 v145, v144

.Lp4a_pad:
.LBB0_428:
	s_mov_b64 s[0:1], 0

.LBB0_594:
	ds_read_b128 v[24:27], v186
	ds_read_b128 v[28:31], v186 offset:1024
	ds_read_b128 v[16:19], v186 offset:2048
	ds_read_b128 v[20:23], v186 offset:3072
	ds_read_b128 v[8:11], v187
	ds_read_b128 v[12:15], v187 offset:1024
	ds_read_b128 v[0:3], v187 offset:2048
	ds_read_b128 v[4:7], v187 offset:3072
	s_add_i32 m0, s31, 0xc000
	ds_read_b128 v[192:195], v188
	ds_read_b128 v[196:199], v188 offset:1024
	ds_read_b128 v[200:203], v188 offset:2048
	ds_read_b128 v[204:207], v188 offset:3072
	ds_read_b128 v[208:211], v188 offset:4096
	ds_read_b128 v[212:215], v188 offset:5120
	ds_read_b128 v[224:227], v188 offset:6144
	ds_read_b128 v[228:231], v188 offset:7168
	global_load_lds_dwordx4 v[178:179], off
	s_add_i32 m0, s31, 0xe000
	s_nop 0
	global_load_lds_dwordx4 v[180:181], off
	s_waitcnt vmcnt(8)
	s_waitcnt lgkmcnt(0)
	s_barrier
	s_setprio 1
	s_waitcnt lgkmcnt(0)
	v_mfma_f32_16x16x128_f8f6f4 v[156:159], v[24:31], v[192:199], v[156:159]
	v_mfma_f32_16x16x128_f8f6f4 v[148:151], v[16:23], v[192:199], v[148:151]
	v_mfma_f32_16x16x128_f8f6f4 v[140:143], v[24:31], v[200:207], v[140:143]
	v_mfma_f32_16x16x128_f8f6f4 v[132:135], v[16:23], v[200:207], v[132:135]
	v_mfma_f32_16x16x128_f8f6f4 v[124:127], v[24:31], v[208:215], v[124:127]
	v_mfma_f32_16x16x128_f8f6f4 v[116:119], v[16:23], v[208:215], v[116:119]
	v_mfma_f32_16x16x128_f8f6f4 v[108:111], v[24:31], v[224:231], v[108:111]
	v_mfma_f32_16x16x128_f8f6f4 v[100:103], v[16:23], v[224:231], v[100:103]
	s_setprio 0
	s_setprio 1
	v_mfma_f32_16x16x128_f8f6f4 v[152:155], v[8:15], v[192:199], v[152:155]
	v_mfma_f32_16x16x128_f8f6f4 v[144:147], v[0:7], v[192:199], v[144:147]
	v_mfma_f32_16x16x128_f8f6f4 v[136:139], v[8:15], v[200:207], v[136:139]
	v_mfma_f32_16x16x128_f8f6f4 v[128:131], v[0:7], v[200:207], v[128:131]
	v_mfma_f32_16x16x128_f8f6f4 v[120:123], v[8:15], v[208:215], v[120:123]
	v_mfma_f32_16x16x128_f8f6f4 v[112:115], v[0:7], v[208:215], v[112:115]
	v_mfma_f32_16x16x128_f8f6f4 v[104:107], v[8:15], v[224:231], v[104:107]
	v_mfma_f32_16x16x128_f8f6f4 v[96:99], v[0:7], v[224:231], v[96:99]
	s_setprio 0
	s_barrier
	s_cmp_gt_u32 s15, 5
	s_cselect_b64 s[36:37], -1, 0
	s_and_b64 s[40:41], s[36:37], exec
	v_sub_co_u32_e64 v216, s[40:41], s15, 6
	s_nop 0
	v_readfirstlane_b32 s73, v216
	s_cselect_b32 s17, s27, s39
	s_cselect_b32 s67, s26, s38
	s_add_i32 s76, s73, 8
	s_and_b64 s[74:75], s[36:37], exec
	s_cselect_b32 s74, s73, s76
	s_ashr_i32 s75, s74, 31
	s_lshl_b64 s[74:75], s[74:75], 7
	s_add_u32 s76, s67, s74
	s_addc_u32 s77, s17, s75
	s_add_i32 s17, s61, s29
	v_lshl_add_u64 v[216:217], s[76:77], 0, v[162:163]
	s_mov_b32 m0, s17
	ds_read_b128 v[192:195], v188 offset:16384
	ds_read_b128 v[196:199], v188 offset:17408
	ds_read_b128 v[200:203], v188 offset:18432
	ds_read_b128 v[204:207], v188 offset:19456
	ds_read_b128 v[208:211], v188 offset:20480
	ds_read_b128 v[212:215], v188 offset:21504
	ds_read_b128 v[224:227], v188 offset:22528
	ds_read_b128 v[228:231], v188 offset:23552
	global_load_lds_dwordx4 v[216:217], off
	s_add_i32 m0, s17, 0x2000
	v_lshl_add_u64 v[216:217], s[76:77], 0, v[166:167]
	s_add_u32 s76, s76, 0x20000
	s_addc_u32 s77, s77, 0
	s_add_i32 s17, s62, s29
	global_load_lds_dwordx4 v[216:217], off
	v_lshl_add_u64 v[216:217], s[76:77], 0, v[162:163]
	s_mov_b32 m0, s17
	s_nop 0
	global_load_lds_dwordx4 v[216:217], off
	s_add_i32 m0, s17, 0x2000
	s_and_b64 s[36:37], s[36:37], exec
	s_cselect_b32 s36, s22, s34
	s_cselect_b32 s17, s23, s35
	s_add_u32 s36, s36, s74
	v_lshl_add_u64 v[216:217], s[76:77], 0, v[166:167]
	s_addc_u32 s37, s17, s75
	global_load_lds_dwordx4 v[216:217], off
	v_lshl_add_u64 v[216:217], s[36:37], 0, v[160:161]
	s_mov_b32 m0, s31
	s_nop 0
	global_load_lds_dwordx4 v[216:217], off
	v_lshl_add_u64 v[216:217], s[36:37], 0, v[164:165]
	s_mov_b32 m0, s49
	s_nop 0
	global_load_lds_dwordx4 v[216:217], off
	s_waitcnt vmcnt(8)
	s_waitcnt lgkmcnt(0)
	s_barrier
	s_setprio 1
	s_waitcnt lgkmcnt(0)
	v_mfma_f32_16x16x128_f8f6f4 v[92:95], v[24:31], v[192:199], v[92:95]
	v_mfma_f32_16x16x128_f8f6f4 v[84:87], v[16:23], v[192:199], v[84:87]
	v_mfma_f32_16x16x128_f8f6f4 v[76:79], v[24:31], v[200:207], v[76:79]
	v_mfma_f32_16x16x128_f8f6f4 v[64:67], v[16:23], v[200:207], v[64:67]
	v_mfma_f32_16x16x128_f8f6f4 v[52:55], v[24:31], v[208:215], v[52:55]
	v_mfma_f32_16x16x128_f8f6f4 v[44:47], v[16:23], v[208:215], v[44:47]
	v_mfma_f32_16x16x128_f8f6f4 v[36:39], v[24:31], v[224:231], v[36:39]
	v_mfma_f32_16x16x128_f8f6f4 v[32:35], v[16:23], v[224:231], v[32:35]
	s_setprio 0
	s_setprio 1
	v_mfma_f32_16x16x128_f8f6f4 v[88:91], v[8:15], v[192:199], v[88:91]
	v_mfma_f32_16x16x128_f8f6f4 v[80:83], v[0:7], v[192:199], v[80:83]
	v_mfma_f32_16x16x128_f8f6f4 v[68:71], v[8:15], v[200:207], v[68:71]
	v_mfma_f32_16x16x128_f8f6f4 v[56:59], v[0:7], v[200:207], v[56:59]
	v_mfma_f32_16x16x128_f8f6f4 v[72:75], v[8:15], v[208:215], v[72:75]
	v_mfma_f32_16x16x128_f8f6f4 v[60:63], v[0:7], v[208:215], v[60:63]
	v_mfma_f32_16x16x128_f8f6f4 v[48:51], v[8:15], v[224:231], v[48:51]
	v_mfma_f32_16x16x128_f8f6f4 v[40:43], v[0:7], v[224:231], v[40:43]
	s_setprio 0
	s_barrier
	s_add_i32 s17, 0, 0x18000
	s_add_i32 s67, 0, 0x1c000
	v_add_u32_e32 v0, s17, v183
	v_add_u32_e32 v4, s67, v183
	ds_read_b128 v[24:27], v0
	ds_read_b128 v[28:31], v0 offset:1024
	ds_read_b128 v[16:19], v0 offset:2048
	ds_read_b128 v[20:23], v0 offset:3072
	ds_read_b128 v[8:11], v4
	ds_read_b128 v[12:15], v4 offset:1024
	ds_read_b128 v[0:3], v4 offset:2048
	ds_read_b128 v[4:7], v4 offset:3072
	s_add_u32 s36, s36, 0x20000
	s_addc_u32 s37, s37, 0
	s_mov_b32 m0, s50
	v_lshl_add_u64 v[216:217], s[36:37], 0, v[160:161]
	ds_read_b128 v[192:195], v188 offset:32768
	ds_read_b128 v[196:199], v188 offset:33792
	ds_read_b128 v[200:203], v188 offset:34816
	ds_read_b128 v[204:207], v188 offset:35840
	ds_read_b128 v[208:211], v188 offset:36864
	ds_read_b128 v[212:215], v188 offset:37888
	ds_read_b128 v[224:227], v188 offset:38912
	ds_read_b128 v[228:231], v188 offset:39936
	global_load_lds_dwordx4 v[216:217], off
	v_lshl_add_u64 v[216:217], s[36:37], 0, v[164:165]
	s_mov_b32 m0, s51
	s_nop 0
	global_load_lds_dwordx4 v[216:217], off
	s_waitcnt vmcnt(8)
	s_waitcnt lgkmcnt(0)
	s_barrier
	s_setprio 1
	s_waitcnt lgkmcnt(0)
	v_mfma_f32_16x16x128_f8f6f4 v[156:159], v[24:31], v[192:199], v[156:159]
	v_mfma_f32_16x16x128_f8f6f4 v[148:151], v[16:23], v[192:199], v[148:151]
	v_mfma_f32_16x16x128_f8f6f4 v[140:143], v[24:31], v[200:207], v[140:143]
	v_mfma_f32_16x16x128_f8f6f4 v[132:135], v[16:23], v[200:207], v[132:135]
	v_mfma_f32_16x16x128_f8f6f4 v[124:127], v[24:31], v[208:215], v[124:127]
	v_mfma_f32_16x16x128_f8f6f4 v[116:119], v[16:23], v[208:215], v[116:119]
	v_mfma_f32_16x16x128_f8f6f4 v[108:111], v[24:31], v[224:231], v[108:111]
	v_mfma_f32_16x16x128_f8f6f4 v[100:103], v[16:23], v[224:231], v[100:103]
	s_setprio 0
	s_setprio 1
	v_mfma_f32_16x16x128_f8f6f4 v[152:155], v[8:15], v[192:199], v[152:155]
	v_mfma_f32_16x16x128_f8f6f4 v[144:147], v[0:7], v[192:199], v[144:147]
	v_mfma_f32_16x16x128_f8f6f4 v[136:139], v[8:15], v[200:207], v[136:139]
	v_mfma_f32_16x16x128_f8f6f4 v[128:131], v[0:7], v[200:207], v[128:131]
	v_mfma_f32_16x16x128_f8f6f4 v[120:123], v[8:15], v[208:215], v[120:123]
	v_mfma_f32_16x16x128_f8f6f4 v[112:115], v[0:7], v[208:215], v[112:115]
	v_mfma_f32_16x16x128_f8f6f4 v[104:107], v[8:15], v[224:231], v[104:107]
	v_mfma_f32_16x16x128_f8f6f4 v[96:99], v[0:7], v[224:231], v[96:99]
	s_setprio 0
	s_barrier
	s_cmp_gt_u32 s15, 4
	s_cselect_b64 s[36:37], -1, 0
	s_and_b64 s[74:75], s[36:37], exec
	s_cselect_b32 s74, -5, 3
	s_cselect_b32 s73, s27, s39
	s_cselect_b32 s76, s26, s38
	s_add_i32 s74, s74, s15
	s_ashr_i32 s75, s74, 31
	s_lshl_b64 s[74:75], s[74:75], 7
	s_add_u32 s76, s76, s74
	s_addc_u32 s77, s73, s75
	s_add_i32 s17, s17, s29
	v_lshl_add_u64 v[216:217], s[76:77], 0, v[162:163]
	s_mov_b32 m0, s17
	ds_read_b128 v[192:195], v188 offset:49152
	ds_read_b128 v[196:199], v188 offset:50176
	ds_read_b128 v[200:203], v188 offset:51200
	ds_read_b128 v[204:207], v188 offset:52224
	ds_read_b128 v[208:211], v188 offset:53248
	ds_read_b128 v[212:215], v188 offset:54272
	ds_read_b128 v[224:227], v188 offset:55296
	ds_read_b128 v[228:231], v188 offset:56320
	global_load_lds_dwordx4 v[216:217], off
	s_add_i32 m0, s17, 0x2000
	v_lshl_add_u64 v[216:217], s[76:77], 0, v[166:167]
	s_add_u32 s76, s76, 0x20000
	s_addc_u32 s77, s77, 0
	s_add_i32 s17, s67, s29
	global_load_lds_dwordx4 v[216:217], off
	v_lshl_add_u64 v[216:217], s[76:77], 0, v[162:163]
	s_mov_b32 m0, s17
	s_nop 0
	global_load_lds_dwordx4 v[216:217], off
	s_add_i32 m0, s17, 0x2000
	s_and_b64 s[36:37], s[36:37], exec
	s_cselect_b32 s36, s22, s34
	s_cselect_b32 s17, s23, s35
	s_add_u32 s36, s36, s74
	v_lshl_add_u64 v[216:217], s[76:77], 0, v[166:167]
	s_addc_u32 s37, s17, s75
	global_load_lds_dwordx4 v[216:217], off
	v_lshl_add_u64 v[216:217], s[36:37], 0, v[160:161]
	s_mov_b32 m0, s56
	s_nop 0
	global_load_lds_dwordx4 v[216:217], off
	v_lshl_add_u64 v[216:217], s[36:37], 0, v[164:165]
	s_mov_b32 m0, s57
	s_nop 0
	global_load_lds_dwordx4 v[216:217], off
	s_waitcnt vmcnt(8)
	s_waitcnt lgkmcnt(0)
	s_barrier
	s_setprio 1
	s_waitcnt lgkmcnt(0)
	v_mfma_f32_16x16x128_f8f6f4 v[92:95], v[24:31], v[192:199], v[92:95]
	v_mfma_f32_16x16x128_f8f6f4 v[84:87], v[16:23], v[192:199], v[84:87]
	v_mfma_f32_16x16x128_f8f6f4 v[76:79], v[24:31], v[200:207], v[76:79]
	v_mfma_f32_16x16x128_f8f6f4 v[64:67], v[16:23], v[200:207], v[64:67]
	v_mfma_f32_16x16x128_f8f6f4 v[52:55], v[24:31], v[208:215], v[52:55]
	v_mfma_f32_16x16x128_f8f6f4 v[44:47], v[16:23], v[208:215], v[44:47]
	v_mfma_f32_16x16x128_f8f6f4 v[36:39], v[24:31], v[224:231], v[36:39]
	v_mfma_f32_16x16x128_f8f6f4 v[32:35], v[16:23], v[224:231], v[32:35]
	s_setprio 0
	s_setprio 1
	v_mfma_f32_16x16x128_f8f6f4 v[88:91], v[8:15], v[192:199], v[88:91]
	v_mfma_f32_16x16x128_f8f6f4 v[80:83], v[0:7], v[192:199], v[80:83]
	v_mfma_f32_16x16x128_f8f6f4 v[68:71], v[8:15], v[200:207], v[68:71]
	v_mfma_f32_16x16x128_f8f6f4 v[56:59], v[0:7], v[200:207], v[56:59]
	v_mfma_f32_16x16x128_f8f6f4 v[72:75], v[8:15], v[208:215], v[72:75]
	v_mfma_f32_16x16x128_f8f6f4 v[60:63], v[0:7], v[208:215], v[60:63]
	v_mfma_f32_16x16x128_f8f6f4 v[48:51], v[8:15], v[224:231], v[48:51]
	v_mfma_f32_16x16x128_f8f6f4 v[40:43], v[0:7], v[224:231], v[40:43]
	s_setprio 0
	s_barrier
	v_lshl_add_u64 v[178:179], v[178:179], 0, s[6:7]
	v_lshl_add_u64 v[180:181], v[180:181], 0, s[6:7]
	s_add_i32 s15, s15, 2
	s_and_b64 vcc, exec, s[40:41]
	s_cbranch_vccnz .LBB0_594
	s_andn2_b64 vcc, exec, s[12:13]
	s_cbranch_vccnz .LBB0_597
	s_barrier

.LBB0_673:
	ds_read_b128 v[24:27], v187
	ds_read_b128 v[28:31], v187 offset:1024
	ds_read_b128 v[16:19], v187 offset:2048
	ds_read_b128 v[20:23], v187 offset:3072
	s_waitcnt lgkmcnt(0)
	ds_read_b128 v[8:11], v188
	ds_read_b128 v[12:15], v188 offset:1024
	ds_read_b128 v[0:3], v188 offset:2048
	ds_read_b128 v[4:7], v188 offset:3072
	s_add_i32 m0, s49, 0xc000
	ds_read_b128 v[192:195], v189
	ds_read_b128 v[196:199], v189 offset:1024
	ds_read_b128 v[200:203], v189 offset:2048
	ds_read_b128 v[204:207], v189 offset:3072
	ds_read_b128 v[208:211], v189 offset:4096
	ds_read_b128 v[212:215], v189 offset:5120
	ds_read_b128 v[224:227], v189 offset:6144
	ds_read_b128 v[228:231], v189 offset:7168
	global_load_lds_dwordx4 v[178:179], off
	s_add_i32 m0, s49, 0xe000
	s_nop 0
	global_load_lds_dwordx4 v[180:181], off
	s_waitcnt vmcnt(8)
	s_waitcnt lgkmcnt(0)
	s_barrier
	s_setprio 1
	s_waitcnt lgkmcnt(0)
	v_mfma_f32_16x16x128_f8f6f4 v[156:159], v[24:31], v[192:199], v[156:159]
	v_mfma_f32_16x16x128_f8f6f4 v[152:155], v[16:23], v[192:199], v[152:155]
	v_mfma_f32_16x16x128_f8f6f4 v[140:143], v[24:31], v[200:207], v[140:143]
	v_mfma_f32_16x16x128_f8f6f4 v[136:139], v[16:23], v[200:207], v[136:139]
	v_mfma_f32_16x16x128_f8f6f4 v[124:127], v[24:31], v[208:215], v[124:127]
	v_mfma_f32_16x16x128_f8f6f4 v[120:123], v[16:23], v[208:215], v[120:123]
	v_mfma_f32_16x16x128_f8f6f4 v[108:111], v[24:31], v[224:231], v[108:111]
	v_mfma_f32_16x16x128_f8f6f4 v[104:107], v[16:23], v[224:231], v[104:107]
	s_setprio 0
	s_setprio 1
	v_mfma_f32_16x16x128_f8f6f4 v[148:151], v[8:15], v[192:199], v[148:151]
	v_mfma_f32_16x16x128_f8f6f4 v[144:147], v[0:7], v[192:199], v[144:147]
	v_mfma_f32_16x16x128_f8f6f4 v[132:135], v[8:15], v[200:207], v[132:135]
	v_mfma_f32_16x16x128_f8f6f4 v[128:131], v[0:7], v[200:207], v[128:131]
	v_mfma_f32_16x16x128_f8f6f4 v[116:119], v[8:15], v[208:215], v[116:119]
	v_mfma_f32_16x16x128_f8f6f4 v[112:115], v[0:7], v[208:215], v[112:115]
	v_mfma_f32_16x16x128_f8f6f4 v[100:103], v[8:15], v[224:231], v[100:103]
	v_mfma_f32_16x16x128_f8f6f4 v[96:99], v[0:7], v[224:231], v[96:99]
	s_setprio 0
	s_barrier
	s_add_i32 s73, s67, 2
	s_cmp_lt_u32 s67, 20
	s_cselect_b64 s[36:37], -1, 0
	s_and_b64 s[74:75], s[36:37], exec
	s_cselect_b32 s0, 0, 0xffffffea
	s_cselect_b32 s77, s29, s39
	s_cselect_b32 s76, s28, s38
	s_add_i32 s0, s73, s0
	s_lshl_b64 s[74:75], s[0:1], 7
	s_add_u32 s76, s76, s74
	s_addc_u32 s77, s77, s75
	s_add_i32 s0, s60, s48
	v_lshl_add_u64 v[216:217], s[76:77], 0, v[162:163]
	s_mov_b32 m0, s0
	ds_read_b128 v[192:195], v189 offset:16384
	ds_read_b128 v[196:199], v189 offset:17408
	ds_read_b128 v[200:203], v189 offset:18432
	ds_read_b128 v[204:207], v189 offset:19456
	ds_read_b128 v[208:211], v189 offset:20480
	ds_read_b128 v[212:215], v189 offset:21504
	ds_read_b128 v[224:227], v189 offset:22528
	ds_read_b128 v[228:231], v189 offset:23552
	global_load_lds_dwordx4 v[216:217], off
	s_add_i32 m0, s0, 0x2000
	v_lshl_add_u64 v[216:217], s[76:77], 0, v[166:167]
	s_add_u32 s76, s76, 0x58000
	s_addc_u32 s77, s77, 0
	s_add_i32 s0, s61, s48
	global_load_lds_dwordx4 v[216:217], off
	v_lshl_add_u64 v[216:217], s[76:77], 0, v[162:163]
	s_mov_b32 m0, s0
	s_nop 0
	global_load_lds_dwordx4 v[216:217], off
	s_add_i32 m0, s0, 0x2000
	s_and_b64 vcc, s[36:37], exec
	s_cselect_b32 s36, s40, s34
	s_cselect_b32 s0, s41, s35
	s_add_u32 s36, s36, s74
	v_lshl_add_u64 v[216:217], s[76:77], 0, v[166:167]
	s_addc_u32 s37, s0, s75
	global_load_lds_dwordx4 v[216:217], off
	v_lshl_add_u64 v[216:217], s[36:37], 0, v[160:161]
	s_mov_b32 m0, s49
	s_nop 0
	global_load_lds_dwordx4 v[216:217], off
	v_lshl_add_u64 v[216:217], s[36:37], 0, v[164:165]
	s_mov_b32 m0, s50
	s_nop 0
	global_load_lds_dwordx4 v[216:217], off
	s_waitcnt vmcnt(8)
	s_waitcnt lgkmcnt(0)
	s_barrier
	s_setprio 1
	s_waitcnt lgkmcnt(0)
	v_mfma_f32_16x16x128_f8f6f4 v[92:95], v[24:31], v[192:199], v[92:95]
	v_mfma_f32_16x16x128_f8f6f4 v[88:91], v[16:23], v[192:199], v[88:91]
	v_mfma_f32_16x16x128_f8f6f4 v[76:79], v[24:31], v[200:207], v[76:79]
	v_mfma_f32_16x16x128_f8f6f4 v[72:75], v[16:23], v[200:207], v[72:75]
	v_mfma_f32_16x16x128_f8f6f4 v[56:59], v[24:31], v[208:215], v[56:59]
	v_mfma_f32_16x16x128_f8f6f4 v[48:51], v[16:23], v[208:215], v[48:51]
	v_mfma_f32_16x16x128_f8f6f4 v[36:39], v[24:31], v[224:231], v[36:39]
	v_mfma_f32_16x16x128_f8f6f4 v[32:35], v[16:23], v[224:231], v[32:35]
	s_setprio 0
	s_setprio 1
	v_mfma_f32_16x16x128_f8f6f4 v[84:87], v[8:15], v[192:199], v[84:87]
	v_mfma_f32_16x16x128_f8f6f4 v[80:83], v[0:7], v[192:199], v[80:83]
	v_mfma_f32_16x16x128_f8f6f4 v[68:71], v[8:15], v[200:207], v[68:71]
	v_mfma_f32_16x16x128_f8f6f4 v[64:67], v[0:7], v[200:207], v[64:67]
	v_mfma_f32_16x16x128_f8f6f4 v[60:63], v[8:15], v[208:215], v[60:63]
	v_mfma_f32_16x16x128_f8f6f4 v[52:55], v[0:7], v[208:215], v[52:55]
	v_mfma_f32_16x16x128_f8f6f4 v[44:47], v[8:15], v[224:231], v[44:47]
	v_mfma_f32_16x16x128_f8f6f4 v[40:43], v[0:7], v[224:231], v[40:43]
	s_setprio 0
	s_barrier
	s_add_i32 s78, 0, 0x18000
	s_add_i32 s79, 0, 0x1c000
	v_add_u32_e32 v0, s78, v183
	v_add_u32_e32 v4, s79, v183
	ds_read_b128 v[24:27], v0
	ds_read_b128 v[28:31], v0 offset:1024
	ds_read_b128 v[16:19], v0 offset:2048
	ds_read_b128 v[20:23], v0 offset:3072
	ds_read_b128 v[8:11], v4
	ds_read_b128 v[12:15], v4 offset:1024
	ds_read_b128 v[0:3], v4 offset:2048
	ds_read_b128 v[4:7], v4 offset:3072
	s_add_u32 s36, s36, 0x58000
	s_addc_u32 s37, s37, 0
	s_mov_b32 m0, s51
	v_lshl_add_u64 v[216:217], s[36:37], 0, v[160:161]
	ds_read_b128 v[192:195], v189 offset:32768
	ds_read_b128 v[196:199], v189 offset:33792
	ds_read_b128 v[200:203], v189 offset:34816
	ds_read_b128 v[204:207], v189 offset:35840
	ds_read_b128 v[208:211], v189 offset:36864
	ds_read_b128 v[212:215], v189 offset:37888
	ds_read_b128 v[224:227], v189 offset:38912
	ds_read_b128 v[228:231], v189 offset:39936
	global_load_lds_dwordx4 v[216:217], off
	v_lshl_add_u64 v[216:217], s[36:37], 0, v[164:165]
	s_mov_b32 m0, s56
	s_nop 0
	global_load_lds_dwordx4 v[216:217], off
	s_waitcnt vmcnt(8)
	s_waitcnt lgkmcnt(0)
	s_barrier
	s_setprio 1
	s_waitcnt lgkmcnt(0)
	v_mfma_f32_16x16x128_f8f6f4 v[156:159], v[24:31], v[192:199], v[156:159]
	v_mfma_f32_16x16x128_f8f6f4 v[152:155], v[16:23], v[192:199], v[152:155]
	v_mfma_f32_16x16x128_f8f6f4 v[140:143], v[24:31], v[200:207], v[140:143]
	v_mfma_f32_16x16x128_f8f6f4 v[136:139], v[16:23], v[200:207], v[136:139]
	v_mfma_f32_16x16x128_f8f6f4 v[124:127], v[24:31], v[208:215], v[124:127]
	v_mfma_f32_16x16x128_f8f6f4 v[120:123], v[16:23], v[208:215], v[120:123]
	v_mfma_f32_16x16x128_f8f6f4 v[108:111], v[24:31], v[224:231], v[108:111]
	v_mfma_f32_16x16x128_f8f6f4 v[104:107], v[16:23], v[224:231], v[104:107]
	s_setprio 0
	s_setprio 1
	v_mfma_f32_16x16x128_f8f6f4 v[148:151], v[8:15], v[192:199], v[148:151]
	v_mfma_f32_16x16x128_f8f6f4 v[144:147], v[0:7], v[192:199], v[144:147]
	v_mfma_f32_16x16x128_f8f6f4 v[132:135], v[8:15], v[200:207], v[132:135]
	v_mfma_f32_16x16x128_f8f6f4 v[128:131], v[0:7], v[200:207], v[128:131]
	v_mfma_f32_16x16x128_f8f6f4 v[116:119], v[8:15], v[208:215], v[116:119]
	v_mfma_f32_16x16x128_f8f6f4 v[112:115], v[0:7], v[208:215], v[112:115]
	v_mfma_f32_16x16x128_f8f6f4 v[100:103], v[8:15], v[224:231], v[100:103]
	v_mfma_f32_16x16x128_f8f6f4 v[96:99], v[0:7], v[224:231], v[96:99]
	s_setprio 0
	s_barrier
	s_cmp_lt_u32 s67, 19
	s_cselect_b64 s[36:37], -1, 0
	s_and_b64 s[74:75], s[36:37], exec
	s_cselect_b32 s0, 0, 0xffffffea
	s_cselect_b32 s77, s29, s39
	s_cselect_b32 s76, s28, s38
	s_add_i32 s0, s0, s67
	s_add_i32 s0, s0, 3
	s_lshl_b64 s[74:75], s[0:1], 7
	s_add_u32 s76, s76, s74
	s_addc_u32 s77, s77, s75
	s_add_i32 s0, s78, s48
	v_lshl_add_u64 v[216:217], s[76:77], 0, v[162:163]
	s_mov_b32 m0, s0
	ds_read_b128 v[192:195], v189 offset:49152
	ds_read_b128 v[196:199], v189 offset:50176
	ds_read_b128 v[200:203], v189 offset:51200
	ds_read_b128 v[204:207], v189 offset:52224
	ds_read_b128 v[208:211], v189 offset:53248
	ds_read_b128 v[212:215], v189 offset:54272
	ds_read_b128 v[224:227], v189 offset:55296
	ds_read_b128 v[228:231], v189 offset:56320
	global_load_lds_dwordx4 v[216:217], off
	s_add_i32 m0, s0, 0x2000
	v_lshl_add_u64 v[216:217], s[76:77], 0, v[166:167]
	s_add_u32 s76, s76, 0x58000
	s_addc_u32 s77, s77, 0
	s_add_i32 s0, s79, s48
	global_load_lds_dwordx4 v[216:217], off
	v_lshl_add_u64 v[216:217], s[76:77], 0, v[162:163]
	s_mov_b32 m0, s0
	s_nop 0
	global_load_lds_dwordx4 v[216:217], off
	s_add_i32 m0, s0, 0x2000
	s_and_b64 s[36:37], s[36:37], exec
	s_cselect_b32 s36, s40, s34
	s_cselect_b32 s0, s41, s35
	s_add_u32 s36, s36, s74
	v_lshl_add_u64 v[216:217], s[76:77], 0, v[166:167]
	s_addc_u32 s37, s0, s75
	global_load_lds_dwordx4 v[216:217], off
	v_lshl_add_u64 v[216:217], s[36:37], 0, v[160:161]
	s_mov_b32 m0, s57
	s_nop 0
	global_load_lds_dwordx4 v[216:217], off
	v_lshl_add_u64 v[216:217], s[36:37], 0, v[164:165]
	s_mov_b32 m0, s58
	s_nop 0
	global_load_lds_dwordx4 v[216:217], off
	s_waitcnt vmcnt(8)
	s_waitcnt lgkmcnt(0)
	s_barrier
	s_setprio 1
	s_waitcnt lgkmcnt(0)
	v_mfma_f32_16x16x128_f8f6f4 v[92:95], v[24:31], v[192:199], v[92:95]
	v_mfma_f32_16x16x128_f8f6f4 v[88:91], v[16:23], v[192:199], v[88:91]
	v_mfma_f32_16x16x128_f8f6f4 v[76:79], v[24:31], v[200:207], v[76:79]
	v_mfma_f32_16x16x128_f8f6f4 v[72:75], v[16:23], v[200:207], v[72:75]
	v_mfma_f32_16x16x128_f8f6f4 v[56:59], v[24:31], v[208:215], v[56:59]
	v_mfma_f32_16x16x128_f8f6f4 v[48:51], v[16:23], v[208:215], v[48:51]
	v_mfma_f32_16x16x128_f8f6f4 v[36:39], v[24:31], v[224:231], v[36:39]
	v_mfma_f32_16x16x128_f8f6f4 v[32:35], v[16:23], v[224:231], v[32:35]
	s_setprio 0
	s_setprio 1
	v_mfma_f32_16x16x128_f8f6f4 v[84:87], v[8:15], v[192:199], v[84:87]
	v_mfma_f32_16x16x128_f8f6f4 v[80:83], v[0:7], v[192:199], v[80:83]
	v_mfma_f32_16x16x128_f8f6f4 v[68:71], v[8:15], v[200:207], v[68:71]
	v_mfma_f32_16x16x128_f8f6f4 v[64:67], v[0:7], v[200:207], v[64:67]
	v_mfma_f32_16x16x128_f8f6f4 v[60:63], v[8:15], v[208:215], v[60:63]
	v_mfma_f32_16x16x128_f8f6f4 v[52:55], v[0:7], v[208:215], v[52:55]
	v_mfma_f32_16x16x128_f8f6f4 v[44:47], v[8:15], v[224:231], v[44:47]
	v_mfma_f32_16x16x128_f8f6f4 v[40:43], v[0:7], v[224:231], v[40:43]
	s_setprio 0
	s_barrier
	v_lshl_add_u64 v[178:179], v[178:179], 0, s[26:27]
	v_lshl_add_u64 v[180:181], v[180:181], 0, s[26:27]
	s_mov_b32 s67, s73
	s_cbranch_vccnz .LBB0_673
	s_andn2_b64 vcc, exec, s[22:23]
	s_cbranch_vccnz .LBB0_676
	s_barrier

.LBB0_746:
	ds_read_b128 v[24:27], v191
	ds_read_b128 v[28:31], v191 offset:1024
	ds_read_b128 v[16:19], v191 offset:2048
	ds_read_b128 v[20:23], v191 offset:3072
	ds_read_b128 v[8:11], v192
	ds_read_b128 v[12:15], v192 offset:1024
	ds_read_b128 v[0:3], v192 offset:2048
	ds_read_b128 v[4:7], v192 offset:3072
	s_add_i32 m0, s29, 0xc000
	ds_read_b128 v[196:199], v193
	ds_read_b128 v[200:203], v193 offset:1024
	ds_read_b128 v[204:207], v193 offset:2048
	ds_read_b128 v[208:211], v193 offset:3072
	ds_read_b128 v[212:215], v193 offset:4096
	ds_read_b128 v[216:219], v193 offset:5120
	ds_read_b128 v[224:227], v193 offset:6144
	ds_read_b128 v[228:231], v193 offset:7168
	global_load_lds_dwordx4 v[180:181], off
	s_add_i32 m0, s29, 0xe000
	s_nop 0
	global_load_lds_dwordx4 v[182:183], off
	s_waitcnt vmcnt(8)
	s_waitcnt lgkmcnt(0)
	s_barrier
	s_setprio 1
	s_waitcnt lgkmcnt(0)
	v_mfma_f32_16x16x128_f8f6f4 v[156:159], v[24:31], v[196:203], v[156:159]
	v_mfma_f32_16x16x128_f8f6f4 v[152:155], v[16:23], v[196:203], v[152:155]
	v_mfma_f32_16x16x128_f8f6f4 v[140:143], v[24:31], v[204:211], v[140:143]
	v_mfma_f32_16x16x128_f8f6f4 v[136:139], v[16:23], v[204:211], v[136:139]
	v_mfma_f32_16x16x128_f8f6f4 v[124:127], v[24:31], v[212:219], v[124:127]
	v_mfma_f32_16x16x128_f8f6f4 v[120:123], v[16:23], v[212:219], v[120:123]
	v_mfma_f32_16x16x128_f8f6f4 v[108:111], v[24:31], v[224:231], v[108:111]
	v_mfma_f32_16x16x128_f8f6f4 v[104:107], v[16:23], v[224:231], v[104:107]
	s_setprio 0
	s_setprio 1
	v_mfma_f32_16x16x128_f8f6f4 v[148:151], v[8:15], v[196:203], v[148:151]
	v_mfma_f32_16x16x128_f8f6f4 v[144:147], v[0:7], v[196:203], v[144:147]
	v_mfma_f32_16x16x128_f8f6f4 v[132:135], v[8:15], v[204:211], v[132:135]
	v_mfma_f32_16x16x128_f8f6f4 v[128:131], v[0:7], v[204:211], v[128:131]
	v_mfma_f32_16x16x128_f8f6f4 v[116:119], v[8:15], v[212:219], v[116:119]
	v_mfma_f32_16x16x128_f8f6f4 v[112:115], v[0:7], v[212:219], v[112:115]
	v_mfma_f32_16x16x128_f8f6f4 v[100:103], v[8:15], v[224:231], v[100:103]
	v_mfma_f32_16x16x128_f8f6f4 v[96:99], v[0:7], v[224:231], v[96:99]
	s_setprio 0
	s_barrier
	s_cmp_gt_u32 s15, 5
	s_cselect_b64 s[36:37], -1, 0
	s_and_b64 s[38:39], s[36:37], exec
	v_sub_co_u32_e64 v168, s[38:39], s15, 6
	s_nop 0
	v_readfirstlane_b32 s74, v168
	s_cselect_b32 s17, s27, s31
	s_cselect_b32 s73, s26, s30
	s_add_i32 s75, s74, 8
	s_and_b64 s[66:67], s[36:37], exec
	s_cselect_b32 s66, s74, s75
	s_ashr_i32 s67, s66, 31
	s_lshl_b64 s[66:67], s[66:67], 7
	s_add_u32 s74, s73, s66
	s_addc_u32 s75, s17, s67
	s_add_i32 s17, s63, s46
	v_lshl_add_u64 v[186:187], s[74:75], 0, v[164:165]
	s_mov_b32 m0, s17
	ds_read_b128 v[196:199], v193 offset:16384
	ds_read_b128 v[200:203], v193 offset:17408
	ds_read_b128 v[204:207], v193 offset:18432
	ds_read_b128 v[208:211], v193 offset:19456
	ds_read_b128 v[212:215], v193 offset:20480
	ds_read_b128 v[216:219], v193 offset:21504
	ds_read_b128 v[224:227], v193 offset:22528
	ds_read_b128 v[228:231], v193 offset:23552
	global_load_lds_dwordx4 v[186:187], off
	s_add_i32 m0, s17, 0x2000
	v_lshl_add_u64 v[186:187], s[74:75], 0, v[160:161]
	s_add_u32 s74, s74, 0x20000
	s_addc_u32 s75, s75, 0
	s_add_i32 s17, s64, s46
	global_load_lds_dwordx4 v[186:187], off
	v_lshl_add_u64 v[186:187], s[74:75], 0, v[164:165]
	s_mov_b32 m0, s17
	s_nop 0
	global_load_lds_dwordx4 v[186:187], off
	s_add_i32 m0, s17, 0x2000
	s_and_b64 s[36:37], s[36:37], exec
	s_cselect_b32 s36, s22, s34
	s_cselect_b32 s17, s23, s35
	s_add_u32 s36, s36, s66
	v_lshl_add_u64 v[186:187], s[74:75], 0, v[160:161]
	s_addc_u32 s37, s17, s67
	global_load_lds_dwordx4 v[186:187], off
	v_lshl_add_u64 v[186:187], s[36:37], 0, v[166:167]
	s_mov_b32 m0, s29
	s_nop 0
	global_load_lds_dwordx4 v[186:187], off
	v_lshl_add_u64 v[186:187], s[36:37], 0, v[162:163]
	s_mov_b32 m0, s49
	s_nop 0
	global_load_lds_dwordx4 v[186:187], off
	s_waitcnt vmcnt(8)
	s_waitcnt lgkmcnt(0)
	s_barrier
	s_setprio 1
	s_waitcnt lgkmcnt(0)
	v_mfma_f32_16x16x128_f8f6f4 v[92:95], v[24:31], v[196:203], v[92:95]
	v_mfma_f32_16x16x128_f8f6f4 v[88:91], v[16:23], v[196:203], v[88:91]
	v_mfma_f32_16x16x128_f8f6f4 v[76:79], v[24:31], v[204:211], v[76:79]
	v_mfma_f32_16x16x128_f8f6f4 v[72:75], v[16:23], v[204:211], v[72:75]
	v_mfma_f32_16x16x128_f8f6f4 v[52:55], v[24:31], v[212:219], v[52:55]
	v_mfma_f32_16x16x128_f8f6f4 v[48:51], v[16:23], v[212:219], v[48:51]
	v_mfma_f32_16x16x128_f8f6f4 v[36:39], v[24:31], v[224:231], v[36:39]
	v_mfma_f32_16x16x128_f8f6f4 v[32:35], v[16:23], v[224:231], v[32:35]
	s_setprio 0
	s_setprio 1
	v_mfma_f32_16x16x128_f8f6f4 v[84:87], v[8:15], v[196:203], v[84:87]
	v_mfma_f32_16x16x128_f8f6f4 v[80:83], v[0:7], v[196:203], v[80:83]
	v_mfma_f32_16x16x128_f8f6f4 v[68:71], v[8:15], v[204:211], v[68:71]
	v_mfma_f32_16x16x128_f8f6f4 v[60:63], v[0:7], v[204:211], v[60:63]
	v_mfma_f32_16x16x128_f8f6f4 v[64:67], v[8:15], v[212:219], v[64:67]
	v_mfma_f32_16x16x128_f8f6f4 v[56:59], v[0:7], v[212:219], v[56:59]
	v_mfma_f32_16x16x128_f8f6f4 v[44:47], v[8:15], v[224:231], v[44:47]
	v_mfma_f32_16x16x128_f8f6f4 v[40:43], v[0:7], v[224:231], v[40:43]
	s_setprio 0
	s_barrier
	s_add_i32 s17, 0, 0x18000
	s_add_i32 s73, 0, 0x1c000
	v_add_u32_e32 v0, s17, v188
	v_add_u32_e32 v4, s73, v188
	ds_read_b128 v[24:27], v0
	ds_read_b128 v[28:31], v0 offset:1024
	ds_read_b128 v[16:19], v0 offset:2048
	ds_read_b128 v[20:23], v0 offset:3072
	ds_read_b128 v[8:11], v4
	ds_read_b128 v[12:15], v4 offset:1024
	ds_read_b128 v[0:3], v4 offset:2048
	ds_read_b128 v[4:7], v4 offset:3072
	s_add_u32 s36, s36, 0x20000
	s_addc_u32 s37, s37, 0
	s_mov_b32 m0, s50
	v_lshl_add_u64 v[186:187], s[36:37], 0, v[166:167]
	ds_read_b128 v[196:199], v193 offset:32768
	ds_read_b128 v[200:203], v193 offset:33792
	ds_read_b128 v[204:207], v193 offset:34816
	ds_read_b128 v[208:211], v193 offset:35840
	ds_read_b128 v[212:215], v193 offset:36864
	ds_read_b128 v[216:219], v193 offset:37888
	ds_read_b128 v[224:227], v193 offset:38912
	ds_read_b128 v[228:231], v193 offset:39936
	global_load_lds_dwordx4 v[186:187], off
	v_lshl_add_u64 v[186:187], s[36:37], 0, v[162:163]
	s_mov_b32 m0, s51
	s_nop 0
	global_load_lds_dwordx4 v[186:187], off
	s_waitcnt vmcnt(8)
	s_waitcnt lgkmcnt(0)
	s_barrier
	s_setprio 1
	s_waitcnt lgkmcnt(0)
	v_mfma_f32_16x16x128_f8f6f4 v[156:159], v[24:31], v[196:203], v[156:159]
	v_mfma_f32_16x16x128_f8f6f4 v[152:155], v[16:23], v[196:203], v[152:155]
	v_mfma_f32_16x16x128_f8f6f4 v[140:143], v[24:31], v[204:211], v[140:143]
	v_mfma_f32_16x16x128_f8f6f4 v[136:139], v[16:23], v[204:211], v[136:139]
	v_mfma_f32_16x16x128_f8f6f4 v[124:127], v[24:31], v[212:219], v[124:127]
	v_mfma_f32_16x16x128_f8f6f4 v[120:123], v[16:23], v[212:219], v[120:123]
	v_mfma_f32_16x16x128_f8f6f4 v[108:111], v[24:31], v[224:231], v[108:111]
	v_mfma_f32_16x16x128_f8f6f4 v[104:107], v[16:23], v[224:231], v[104:107]
	s_setprio 0
	s_setprio 1
	v_mfma_f32_16x16x128_f8f6f4 v[148:151], v[8:15], v[196:203], v[148:151]
	v_mfma_f32_16x16x128_f8f6f4 v[144:147], v[0:7], v[196:203], v[144:147]
	v_mfma_f32_16x16x128_f8f6f4 v[132:135], v[8:15], v[204:211], v[132:135]
	v_mfma_f32_16x16x128_f8f6f4 v[128:131], v[0:7], v[204:211], v[128:131]
	v_mfma_f32_16x16x128_f8f6f4 v[116:119], v[8:15], v[212:219], v[116:119]
	v_mfma_f32_16x16x128_f8f6f4 v[112:115], v[0:7], v[212:219], v[112:115]
	v_mfma_f32_16x16x128_f8f6f4 v[100:103], v[8:15], v[224:231], v[100:103]
	v_mfma_f32_16x16x128_f8f6f4 v[96:99], v[0:7], v[224:231], v[96:99]
	s_setprio 0
	s_barrier
	s_cmp_gt_u32 s15, 4
	s_cselect_b64 s[36:37], -1, 0
	s_and_b64 s[66:67], s[36:37], exec
	s_cselect_b32 s66, -5, 3
	s_cselect_b32 s75, s27, s31
	s_cselect_b32 s74, s26, s30
	s_add_i32 s66, s66, s15
	s_ashr_i32 s67, s66, 31
	s_lshl_b64 s[66:67], s[66:67], 7
	s_add_u32 s74, s74, s66
	s_addc_u32 s75, s75, s67
	s_add_i32 s17, s17, s46
	v_lshl_add_u64 v[186:187], s[74:75], 0, v[164:165]
	s_mov_b32 m0, s17
	ds_read_b128 v[196:199], v193 offset:49152
	ds_read_b128 v[200:203], v193 offset:50176
	ds_read_b128 v[204:207], v193 offset:51200
	ds_read_b128 v[208:211], v193 offset:52224
	ds_read_b128 v[212:215], v193 offset:53248
	ds_read_b128 v[216:219], v193 offset:54272
	ds_read_b128 v[224:227], v193 offset:55296
	ds_read_b128 v[228:231], v193 offset:56320
	global_load_lds_dwordx4 v[186:187], off
	s_add_i32 m0, s17, 0x2000
	v_lshl_add_u64 v[186:187], s[74:75], 0, v[160:161]
	s_add_u32 s74, s74, 0x20000
	s_addc_u32 s75, s75, 0
	s_add_i32 s17, s73, s46
	global_load_lds_dwordx4 v[186:187], off
	v_lshl_add_u64 v[186:187], s[74:75], 0, v[164:165]
	s_mov_b32 m0, s17
	s_nop 0
	global_load_lds_dwordx4 v[186:187], off
	s_add_i32 m0, s17, 0x2000
	s_and_b64 s[36:37], s[36:37], exec
	s_cselect_b32 s36, s22, s34
	s_cselect_b32 s17, s23, s35
	s_add_u32 s36, s36, s66
	v_lshl_add_u64 v[186:187], s[74:75], 0, v[160:161]
	s_addc_u32 s37, s17, s67
	global_load_lds_dwordx4 v[186:187], off
	v_lshl_add_u64 v[186:187], s[36:37], 0, v[166:167]
	s_mov_b32 m0, s59
	s_nop 0
	global_load_lds_dwordx4 v[186:187], off
	v_lshl_add_u64 v[186:187], s[36:37], 0, v[162:163]
	s_mov_b32 m0, s60
	s_nop 0
	global_load_lds_dwordx4 v[186:187], off
	s_waitcnt vmcnt(8)
	s_waitcnt lgkmcnt(0)
	s_barrier
	s_setprio 1
	s_waitcnt lgkmcnt(0)
	v_mfma_f32_16x16x128_f8f6f4 v[92:95], v[24:31], v[196:203], v[92:95]
	v_mfma_f32_16x16x128_f8f6f4 v[88:91], v[16:23], v[196:203], v[88:91]
	v_mfma_f32_16x16x128_f8f6f4 v[76:79], v[24:31], v[204:211], v[76:79]
	v_mfma_f32_16x16x128_f8f6f4 v[72:75], v[16:23], v[204:211], v[72:75]
	v_mfma_f32_16x16x128_f8f6f4 v[52:55], v[24:31], v[212:219], v[52:55]
	v_mfma_f32_16x16x128_f8f6f4 v[48:51], v[16:23], v[212:219], v[48:51]
	v_mfma_f32_16x16x128_f8f6f4 v[36:39], v[24:31], v[224:231], v[36:39]
	v_mfma_f32_16x16x128_f8f6f4 v[32:35], v[16:23], v[224:231], v[32:35]
	s_setprio 0
	s_setprio 1
	v_mfma_f32_16x16x128_f8f6f4 v[84:87], v[8:15], v[196:203], v[84:87]
	v_mfma_f32_16x16x128_f8f6f4 v[80:83], v[0:7], v[196:203], v[80:83]
	v_mfma_f32_16x16x128_f8f6f4 v[68:71], v[8:15], v[204:211], v[68:71]
	v_mfma_f32_16x16x128_f8f6f4 v[60:63], v[0:7], v[204:211], v[60:63]
	v_mfma_f32_16x16x128_f8f6f4 v[64:67], v[8:15], v[212:219], v[64:67]
	v_mfma_f32_16x16x128_f8f6f4 v[56:59], v[0:7], v[212:219], v[56:59]
	v_mfma_f32_16x16x128_f8f6f4 v[44:47], v[8:15], v[224:231], v[44:47]
	v_mfma_f32_16x16x128_f8f6f4 v[40:43], v[0:7], v[224:231], v[40:43]
	s_setprio 0
	s_barrier
	v_lshl_add_u64 v[180:181], v[180:181], 0, s[12:13]
	v_lshl_add_u64 v[182:183], v[182:183], 0, s[12:13]
	s_add_i32 s15, s15, 2
	s_and_b64 vcc, exec, s[38:39]
	s_cbranch_vccnz .LBB0_746
	s_andn2_b64 vcc, exec, s[8:9]
	s_cbranch_vccnz .LBB0_749
	s_barrier

.LBB0_773:
	ds_read_b128 v[24:27], v200
	ds_read_b128 v[28:31], v200 offset:1024
	ds_read_b128 v[16:19], v200 offset:2048
	ds_read_b128 v[20:23], v200 offset:3072
	ds_read_b128 v[8:11], v201
	ds_read_b128 v[12:15], v201 offset:1024
	ds_read_b128 v[0:3], v201 offset:2048
	ds_read_b128 v[4:7], v201 offset:3072
	s_add_i32 m0, s39, 0xc000
	ds_read_b128 v[206:209], v202
	ds_read_b128 v[210:213], v202 offset:1024
	ds_read_b128 v[214:217], v202 offset:2048
	ds_read_b128 v[218:221], v202 offset:3072
	ds_read_b128 v[224:227], v202 offset:4096
	ds_read_b128 v[228:231], v202 offset:5120
	ds_read_b128 v[232:235], v202 offset:6144
	ds_read_b128 v[236:239], v202 offset:7168
	global_load_lds_dwordx4 v[194:195], off
	s_add_i32 m0, s39, 0xe000
	s_nop 0
	global_load_lds_dwordx4 v[196:197], off
	s_waitcnt vmcnt(8)
	s_waitcnt lgkmcnt(0)
	s_barrier
	s_setprio 1
	s_waitcnt lgkmcnt(0)
	v_mfma_f32_16x16x128_f8f6f4 v[156:159], v[24:31], v[206:213], v[156:159]
	v_mfma_f32_16x16x128_f8f6f4 v[152:155], v[16:23], v[206:213], v[152:155]
	v_mfma_f32_16x16x128_f8f6f4 v[144:147], v[24:31], v[214:221], v[144:147]
	v_mfma_f32_16x16x128_f8f6f4 v[136:139], v[16:23], v[214:221], v[136:139]
	v_mfma_f32_16x16x128_f8f6f4 v[128:131], v[24:31], v[224:231], v[128:131]
	v_mfma_f32_16x16x128_f8f6f4 v[120:123], v[16:23], v[224:231], v[120:123]
	v_mfma_f32_16x16x128_f8f6f4 v[112:115], v[24:31], v[232:239], v[112:115]
	v_mfma_f32_16x16x128_f8f6f4 v[104:107], v[16:23], v[232:239], v[104:107]
	s_setprio 0
	s_setprio 1
	v_mfma_f32_16x16x128_f8f6f4 v[148:151], v[8:15], v[206:213], v[148:151]
	v_mfma_f32_16x16x128_f8f6f4 v[140:143], v[0:7], v[206:213], v[140:143]
	v_mfma_f32_16x16x128_f8f6f4 v[132:135], v[8:15], v[214:221], v[132:135]
	v_mfma_f32_16x16x128_f8f6f4 v[124:127], v[0:7], v[214:221], v[124:127]
	v_mfma_f32_16x16x128_f8f6f4 v[116:119], v[8:15], v[224:231], v[116:119]
	v_mfma_f32_16x16x128_f8f6f4 v[108:111], v[0:7], v[224:231], v[108:111]
	v_mfma_f32_16x16x128_f8f6f4 v[100:103], v[8:15], v[232:239], v[100:103]
	v_mfma_f32_16x16x128_f8f6f4 v[96:99], v[0:7], v[232:239], v[96:99]
	s_setprio 0
	s_barrier
	s_cmp_gt_u32 s9, 5
	s_cselect_b64 s[34:35], -1, 0
	s_and_b64 s[30:31], s[34:35], exec
	v_sub_co_u32_e64 v205, s[30:31], s9, 6
	s_nop 0
	v_readfirstlane_b32 s63, v205
	s_cselect_b32 s17, s23, s27
	s_cselect_b32 s62, s22, s26
	s_add_i32 s64, s63, 8
	s_and_b64 s[60:61], s[34:35], exec
	s_cselect_b32 s60, s63, s64
	s_ashr_i32 s61, s60, 31
	s_lshl_b64 s[60:61], s[60:61], 7
	s_add_u32 s62, s62, s60
	s_addc_u32 s63, s17, s61
	s_add_i32 s17, s57, s38
	v_lshl_add_u64 v[222:223], s[62:63], 0, v[162:163]
	s_mov_b32 m0, s17
	ds_read_b128 v[206:209], v202 offset:16384
	ds_read_b128 v[210:213], v202 offset:17408
	ds_read_b128 v[214:217], v202 offset:18432
	ds_read_b128 v[218:221], v202 offset:19456
	ds_read_b128 v[224:227], v202 offset:20480
	ds_read_b128 v[228:231], v202 offset:21504
	ds_read_b128 v[232:235], v202 offset:22528
	ds_read_b128 v[236:239], v202 offset:23552
	global_load_lds_dwordx4 v[222:223], off
	s_add_i32 m0, s17, 0x2000
	v_lshl_add_u64 v[222:223], s[62:63], 0, v[166:167]
	s_add_u32 s62, s62, 0x20000
	s_addc_u32 s63, s63, 0
	s_add_i32 s17, s58, s38
	global_load_lds_dwordx4 v[222:223], off
	v_lshl_add_u64 v[222:223], s[62:63], 0, v[162:163]
	s_mov_b32 m0, s17
	s_nop 0
	global_load_lds_dwordx4 v[222:223], off
	s_add_i32 m0, s17, 0x2000
	s_and_b64 s[34:35], s[34:35], exec
	s_cselect_b32 s34, s18, s28
	s_cselect_b32 s17, s19, s29
	s_add_u32 s34, s34, s60
	v_lshl_add_u64 v[222:223], s[62:63], 0, v[166:167]
	s_addc_u32 s35, s17, s61
	global_load_lds_dwordx4 v[222:223], off
	v_lshl_add_u64 v[222:223], s[34:35], 0, v[160:161]
	s_mov_b32 m0, s39
	s_nop 0
	global_load_lds_dwordx4 v[222:223], off
	v_lshl_add_u64 v[222:223], s[34:35], 0, v[164:165]
	s_mov_b32 m0, s42
	s_nop 0
	global_load_lds_dwordx4 v[222:223], off
	s_waitcnt vmcnt(8)
	s_waitcnt lgkmcnt(0)
	s_barrier
	s_setprio 1
	s_waitcnt lgkmcnt(0)
	v_mfma_f32_16x16x128_f8f6f4 v[92:95], v[24:31], v[206:213], v[92:95]
	v_mfma_f32_16x16x128_f8f6f4 v[88:91], v[16:23], v[206:213], v[88:91]
	v_mfma_f32_16x16x128_f8f6f4 v[80:83], v[24:31], v[214:221], v[80:83]
	v_mfma_f32_16x16x128_f8f6f4 v[64:67], v[16:23], v[214:221], v[64:67]
	v_mfma_f32_16x16x128_f8f6f4 v[48:51], v[24:31], v[224:231], v[48:51]
	v_mfma_f32_16x16x128_f8f6f4 v[40:43], v[16:23], v[224:231], v[40:43]
	v_mfma_f32_16x16x128_f8f6f4 v[36:39], v[24:31], v[232:239], v[36:39]
	v_mfma_f32_16x16x128_f8f6f4 v[32:35], v[16:23], v[232:239], v[32:35]
	s_setprio 0
	s_setprio 1
	v_mfma_f32_16x16x128_f8f6f4 v[84:87], v[8:15], v[206:213], v[84:87]
	v_mfma_f32_16x16x128_f8f6f4 v[76:79], v[0:7], v[206:213], v[76:79]
	v_mfma_f32_16x16x128_f8f6f4 v[52:55], v[8:15], v[214:221], v[52:55]
	v_mfma_f32_16x16x128_f8f6f4 v[44:47], v[0:7], v[214:221], v[44:47]
	v_mfma_f32_16x16x128_f8f6f4 v[72:75], v[8:15], v[224:231], v[72:75]
	v_mfma_f32_16x16x128_f8f6f4 v[68:71], v[0:7], v[224:231], v[68:71]
	v_mfma_f32_16x16x128_f8f6f4 v[60:63], v[8:15], v[232:239], v[60:63]
	v_mfma_f32_16x16x128_f8f6f4 v[56:59], v[0:7], v[232:239], v[56:59]
	s_setprio 0
	s_barrier
	s_add_i32 s17, 0, 0x18000
	s_add_i32 s64, 0, 0x1c000
	v_add_u32_e32 v0, s17, v198
	v_add_u32_e32 v4, s64, v198
	ds_read_b128 v[24:27], v0
	ds_read_b128 v[28:31], v0 offset:1024
	ds_read_b128 v[16:19], v0 offset:2048
	ds_read_b128 v[20:23], v0 offset:3072
	ds_read_b128 v[8:11], v4
	ds_read_b128 v[12:15], v4 offset:1024
	ds_read_b128 v[0:3], v4 offset:2048
	ds_read_b128 v[4:7], v4 offset:3072
	s_add_u32 s34, s34, 0x20000
	s_addc_u32 s35, s35, 0
	s_mov_b32 m0, s43
	v_lshl_add_u64 v[222:223], s[34:35], 0, v[160:161]
	ds_read_b128 v[206:209], v202 offset:32768
	ds_read_b128 v[210:213], v202 offset:33792
	ds_read_b128 v[214:217], v202 offset:34816
	ds_read_b128 v[218:221], v202 offset:35840
	ds_read_b128 v[224:227], v202 offset:36864
	ds_read_b128 v[228:231], v202 offset:37888
	ds_read_b128 v[232:235], v202 offset:38912
	ds_read_b128 v[236:239], v202 offset:39936
	global_load_lds_dwordx4 v[222:223], off
	v_lshl_add_u64 v[222:223], s[34:35], 0, v[164:165]
	s_mov_b32 m0, s46
	s_nop 0
	global_load_lds_dwordx4 v[222:223], off
	s_waitcnt vmcnt(8)
	s_waitcnt lgkmcnt(0)
	s_barrier
	s_setprio 1
	s_waitcnt lgkmcnt(0)
	v_mfma_f32_16x16x128_f8f6f4 v[156:159], v[24:31], v[206:213], v[156:159]
	v_mfma_f32_16x16x128_f8f6f4 v[152:155], v[16:23], v[206:213], v[152:155]
	v_mfma_f32_16x16x128_f8f6f4 v[144:147], v[24:31], v[214:221], v[144:147]
	v_mfma_f32_16x16x128_f8f6f4 v[136:139], v[16:23], v[214:221], v[136:139]
	v_mfma_f32_16x16x128_f8f6f4 v[128:131], v[24:31], v[224:231], v[128:131]
	v_mfma_f32_16x16x128_f8f6f4 v[120:123], v[16:23], v[224:231], v[120:123]
	v_mfma_f32_16x16x128_f8f6f4 v[112:115], v[24:31], v[232:239], v[112:115]
	v_mfma_f32_16x16x128_f8f6f4 v[104:107], v[16:23], v[232:239], v[104:107]
	s_setprio 0
	s_setprio 1
	v_mfma_f32_16x16x128_f8f6f4 v[148:151], v[8:15], v[206:213], v[148:151]
	v_mfma_f32_16x16x128_f8f6f4 v[140:143], v[0:7], v[206:213], v[140:143]
	v_mfma_f32_16x16x128_f8f6f4 v[132:135], v[8:15], v[214:221], v[132:135]
	v_mfma_f32_16x16x128_f8f6f4 v[124:127], v[0:7], v[214:221], v[124:127]
	v_mfma_f32_16x16x128_f8f6f4 v[116:119], v[8:15], v[224:231], v[116:119]
	v_mfma_f32_16x16x128_f8f6f4 v[108:111], v[0:7], v[224:231], v[108:111]
	v_mfma_f32_16x16x128_f8f6f4 v[100:103], v[8:15], v[232:239], v[100:103]
	v_mfma_f32_16x16x128_f8f6f4 v[96:99], v[0:7], v[232:239], v[96:99]
	s_setprio 0
	s_barrier
	s_cmp_gt_u32 s9, 4
	s_cselect_b64 s[34:35], -1, 0
	s_and_b64 s[60:61], s[34:35], exec
	s_cselect_b32 s60, -5, 3
	s_cselect_b32 s63, s23, s27
	s_cselect_b32 s62, s22, s26
	s_add_i32 s60, s60, s9
	s_ashr_i32 s61, s60, 31
	s_lshl_b64 s[60:61], s[60:61], 7
	s_add_u32 s62, s62, s60
	s_addc_u32 s63, s63, s61
	s_add_i32 s17, s17, s38
	v_lshl_add_u64 v[222:223], s[62:63], 0, v[162:163]
	s_mov_b32 m0, s17
	ds_read_b128 v[206:209], v202 offset:49152
	ds_read_b128 v[210:213], v202 offset:50176
	ds_read_b128 v[214:217], v202 offset:51200
	ds_read_b128 v[218:221], v202 offset:52224
	ds_read_b128 v[224:227], v202 offset:53248
	ds_read_b128 v[228:231], v202 offset:54272
	ds_read_b128 v[232:235], v202 offset:55296
	ds_read_b128 v[236:239], v202 offset:56320
	global_load_lds_dwordx4 v[222:223], off
	s_add_i32 m0, s17, 0x2000
	v_lshl_add_u64 v[222:223], s[62:63], 0, v[166:167]
	s_add_u32 s62, s62, 0x20000
	s_addc_u32 s63, s63, 0
	s_add_i32 s17, s64, s38
	global_load_lds_dwordx4 v[222:223], off
	v_lshl_add_u64 v[222:223], s[62:63], 0, v[162:163]
	s_mov_b32 m0, s17
	s_nop 0
	global_load_lds_dwordx4 v[222:223], off
	s_add_i32 m0, s17, 0x2000
	s_and_b64 s[34:35], s[34:35], exec
	s_cselect_b32 s34, s18, s28
	s_cselect_b32 s17, s19, s29
	s_add_u32 s34, s34, s60
	v_lshl_add_u64 v[222:223], s[62:63], 0, v[166:167]
	s_addc_u32 s35, s17, s61
	global_load_lds_dwordx4 v[222:223], off
	v_lshl_add_u64 v[222:223], s[34:35], 0, v[160:161]
	s_mov_b32 m0, s49
	s_nop 0
	global_load_lds_dwordx4 v[222:223], off
	v_lshl_add_u64 v[222:223], s[34:35], 0, v[164:165]
	s_mov_b32 m0, s50
	s_nop 0
	global_load_lds_dwordx4 v[222:223], off
	s_waitcnt vmcnt(8)
	s_waitcnt lgkmcnt(0)
	s_barrier
	s_setprio 1
	s_waitcnt lgkmcnt(0)
	v_mfma_f32_16x16x128_f8f6f4 v[92:95], v[24:31], v[206:213], v[92:95]
	v_mfma_f32_16x16x128_f8f6f4 v[88:91], v[16:23], v[206:213], v[88:91]
	v_mfma_f32_16x16x128_f8f6f4 v[80:83], v[24:31], v[214:221], v[80:83]
	v_mfma_f32_16x16x128_f8f6f4 v[64:67], v[16:23], v[214:221], v[64:67]
	v_mfma_f32_16x16x128_f8f6f4 v[48:51], v[24:31], v[224:231], v[48:51]
	v_mfma_f32_16x16x128_f8f6f4 v[40:43], v[16:23], v[224:231], v[40:43]
	v_mfma_f32_16x16x128_f8f6f4 v[36:39], v[24:31], v[232:239], v[36:39]
	v_mfma_f32_16x16x128_f8f6f4 v[32:35], v[16:23], v[232:239], v[32:35]
	s_setprio 0
	s_setprio 1
	v_mfma_f32_16x16x128_f8f6f4 v[84:87], v[8:15], v[206:213], v[84:87]
	v_mfma_f32_16x16x128_f8f6f4 v[76:79], v[0:7], v[206:213], v[76:79]
	v_mfma_f32_16x16x128_f8f6f4 v[52:55], v[8:15], v[214:221], v[52:55]
	v_mfma_f32_16x16x128_f8f6f4 v[44:47], v[0:7], v[214:221], v[44:47]
	v_mfma_f32_16x16x128_f8f6f4 v[72:75], v[8:15], v[224:231], v[72:75]
	v_mfma_f32_16x16x128_f8f6f4 v[68:71], v[0:7], v[224:231], v[68:71]
	v_mfma_f32_16x16x128_f8f6f4 v[60:63], v[8:15], v[232:239], v[60:63]
	v_mfma_f32_16x16x128_f8f6f4 v[56:59], v[0:7], v[232:239], v[56:59]
	s_setprio 0
	s_barrier
	v_lshl_add_u64 v[194:195], v[194:195], 0, s[12:13]
	v_lshl_add_u64 v[196:197], v[196:197], 0, s[12:13]
	s_add_i32 s9, s9, 2
	s_and_b64 vcc, exec, s[30:31]
	s_cbranch_vccnz .LBB0_773
	s_andn2_b64 vcc, exec, s[10:11]
	s_cbranch_vccnz .LBB0_776
	s_barrier

.LBB0_959:
	ds_read_b128 v[24:27], v187
	ds_read_b128 v[28:31], v187 offset:1024
	ds_read_b128 v[16:19], v187 offset:2048
	ds_read_b128 v[20:23], v187 offset:3072
	s_waitcnt lgkmcnt(0)
	ds_read_b128 v[8:11], v188
	ds_read_b128 v[12:15], v188 offset:1024
	ds_read_b128 v[0:3], v188 offset:2048
	ds_read_b128 v[4:7], v188 offset:3072
	s_add_i32 m0, s49, 0xc000
	ds_read_b128 v[192:195], v189
	ds_read_b128 v[196:199], v189 offset:1024
	ds_read_b128 v[200:203], v189 offset:2048
	ds_read_b128 v[204:207], v189 offset:3072
	ds_read_b128 v[208:211], v189 offset:4096
	ds_read_b128 v[212:215], v189 offset:5120
	ds_read_b128 v[224:227], v189 offset:6144
	ds_read_b128 v[228:231], v189 offset:7168
	global_load_lds_dwordx4 v[178:179], off
	s_add_i32 m0, s49, 0xe000
	s_nop 0
	global_load_lds_dwordx4 v[180:181], off
	s_waitcnt vmcnt(8)
	s_waitcnt lgkmcnt(0)
	s_barrier
	s_setprio 1
	s_waitcnt lgkmcnt(0)
	v_mfma_f32_16x16x128_f8f6f4 v[156:159], v[24:31], v[192:199], v[156:159]
	v_mfma_f32_16x16x128_f8f6f4 v[152:155], v[16:23], v[192:199], v[152:155]
	v_mfma_f32_16x16x128_f8f6f4 v[140:143], v[24:31], v[200:207], v[140:143]
	v_mfma_f32_16x16x128_f8f6f4 v[136:139], v[16:23], v[200:207], v[136:139]
	v_mfma_f32_16x16x128_f8f6f4 v[124:127], v[24:31], v[208:215], v[124:127]
	v_mfma_f32_16x16x128_f8f6f4 v[120:123], v[16:23], v[208:215], v[120:123]
	v_mfma_f32_16x16x128_f8f6f4 v[108:111], v[24:31], v[224:231], v[108:111]
	v_mfma_f32_16x16x128_f8f6f4 v[104:107], v[16:23], v[224:231], v[104:107]
	s_setprio 0
	s_setprio 1
	v_mfma_f32_16x16x128_f8f6f4 v[148:151], v[8:15], v[192:199], v[148:151]
	v_mfma_f32_16x16x128_f8f6f4 v[144:147], v[0:7], v[192:199], v[144:147]
	v_mfma_f32_16x16x128_f8f6f4 v[132:135], v[8:15], v[200:207], v[132:135]
	v_mfma_f32_16x16x128_f8f6f4 v[128:131], v[0:7], v[200:207], v[128:131]
	v_mfma_f32_16x16x128_f8f6f4 v[116:119], v[8:15], v[208:215], v[116:119]
	v_mfma_f32_16x16x128_f8f6f4 v[112:115], v[0:7], v[208:215], v[112:115]
	v_mfma_f32_16x16x128_f8f6f4 v[100:103], v[8:15], v[224:231], v[100:103]
	v_mfma_f32_16x16x128_f8f6f4 v[96:99], v[0:7], v[224:231], v[96:99]
	s_setprio 0
	s_barrier
	s_add_i32 s23, s21, 2
	s_cmp_lt_u32 s21, 6
	s_cselect_b64 s[36:37], -1, 0
	s_and_b64 s[64:65], s[36:37], exec
	s_cselect_b32 s0, 0, -8
	s_cselect_b32 s63, s39, s35
	s_cselect_b32 s66, s38, s34
	s_add_i32 s0, s23, s0
	s_lshl_b64 s[64:65], s[0:1], 7
	s_add_u32 s66, s66, s64
	s_addc_u32 s67, s63, s65
	s_add_i32 s0, s60, s48
	v_lshl_add_u64 v[216:217], s[66:67], 0, v[162:163]
	s_mov_b32 m0, s0
	ds_read_b128 v[192:195], v189 offset:16384
	ds_read_b128 v[196:199], v189 offset:17408
	ds_read_b128 v[200:203], v189 offset:18432
	ds_read_b128 v[204:207], v189 offset:19456
	ds_read_b128 v[208:211], v189 offset:20480
	ds_read_b128 v[212:215], v189 offset:21504
	ds_read_b128 v[224:227], v189 offset:22528
	ds_read_b128 v[228:231], v189 offset:23552
	global_load_lds_dwordx4 v[216:217], off
	s_add_i32 m0, s0, 0x2000
	v_lshl_add_u64 v[216:217], s[66:67], 0, v[166:167]
	s_add_u32 s66, s66, 0x20000
	s_addc_u32 s67, s67, 0
	s_add_i32 s0, s61, s48
	global_load_lds_dwordx4 v[216:217], off
	v_lshl_add_u64 v[216:217], s[66:67], 0, v[162:163]
	s_mov_b32 m0, s0
	s_nop 0
	global_load_lds_dwordx4 v[216:217], off
	s_add_i32 m0, s0, 0x2000
	s_and_b64 vcc, s[36:37], exec
	s_cselect_b32 s36, s40, s30
	s_cselect_b32 s0, s41, s31
	s_add_u32 s36, s36, s64
	v_lshl_add_u64 v[216:217], s[66:67], 0, v[166:167]
	s_addc_u32 s37, s0, s65
	global_load_lds_dwordx4 v[216:217], off
	v_lshl_add_u64 v[216:217], s[36:37], 0, v[160:161]
	s_mov_b32 m0, s49
	s_nop 0
	global_load_lds_dwordx4 v[216:217], off
	v_lshl_add_u64 v[216:217], s[36:37], 0, v[164:165]
	s_mov_b32 m0, s50
	s_nop 0
	global_load_lds_dwordx4 v[216:217], off
	s_waitcnt vmcnt(8)
	s_waitcnt lgkmcnt(0)
	s_barrier
	s_setprio 1
	s_waitcnt lgkmcnt(0)
	v_mfma_f32_16x16x128_f8f6f4 v[92:95], v[24:31], v[192:199], v[92:95]
	v_mfma_f32_16x16x128_f8f6f4 v[88:91], v[16:23], v[192:199], v[88:91]
	v_mfma_f32_16x16x128_f8f6f4 v[76:79], v[24:31], v[200:207], v[76:79]
	v_mfma_f32_16x16x128_f8f6f4 v[72:75], v[16:23], v[200:207], v[72:75]
	v_mfma_f32_16x16x128_f8f6f4 v[56:59], v[24:31], v[208:215], v[56:59]
	v_mfma_f32_16x16x128_f8f6f4 v[48:51], v[16:23], v[208:215], v[48:51]
	v_mfma_f32_16x16x128_f8f6f4 v[36:39], v[24:31], v[224:231], v[36:39]
	v_mfma_f32_16x16x128_f8f6f4 v[32:35], v[16:23], v[224:231], v[32:35]
	s_setprio 0
	s_setprio 1
	v_mfma_f32_16x16x128_f8f6f4 v[84:87], v[8:15], v[192:199], v[84:87]
	v_mfma_f32_16x16x128_f8f6f4 v[80:83], v[0:7], v[192:199], v[80:83]
	v_mfma_f32_16x16x128_f8f6f4 v[68:71], v[8:15], v[200:207], v[68:71]
	v_mfma_f32_16x16x128_f8f6f4 v[64:67], v[0:7], v[200:207], v[64:67]
	v_mfma_f32_16x16x128_f8f6f4 v[60:63], v[8:15], v[208:215], v[60:63]
	v_mfma_f32_16x16x128_f8f6f4 v[52:55], v[0:7], v[208:215], v[52:55]
	v_mfma_f32_16x16x128_f8f6f4 v[44:47], v[8:15], v[224:231], v[44:47]
	v_mfma_f32_16x16x128_f8f6f4 v[40:43], v[0:7], v[224:231], v[40:43]
	s_setprio 0
	s_barrier
	s_add_i32 s63, 0, 0x18000
	s_add_i32 s68, 0, 0x1c000
	v_add_u32_e32 v0, s63, v183
	v_add_u32_e32 v4, s68, v183
	ds_read_b128 v[24:27], v0
	ds_read_b128 v[28:31], v0 offset:1024
	ds_read_b128 v[16:19], v0 offset:2048
	ds_read_b128 v[20:23], v0 offset:3072
	ds_read_b128 v[8:11], v4
	ds_read_b128 v[12:15], v4 offset:1024
	ds_read_b128 v[0:3], v4 offset:2048
	ds_read_b128 v[4:7], v4 offset:3072
	s_add_u32 s36, s36, 0x20000
	s_addc_u32 s37, s37, 0
	s_mov_b32 m0, s51
	v_lshl_add_u64 v[216:217], s[36:37], 0, v[160:161]
	ds_read_b128 v[192:195], v189 offset:32768
	ds_read_b128 v[196:199], v189 offset:33792
	ds_read_b128 v[200:203], v189 offset:34816
	ds_read_b128 v[204:207], v189 offset:35840
	ds_read_b128 v[208:211], v189 offset:36864
	ds_read_b128 v[212:215], v189 offset:37888
	ds_read_b128 v[224:227], v189 offset:38912
	ds_read_b128 v[228:231], v189 offset:39936
	global_load_lds_dwordx4 v[216:217], off
	v_lshl_add_u64 v[216:217], s[36:37], 0, v[164:165]
	s_mov_b32 m0, s56
	s_nop 0
	global_load_lds_dwordx4 v[216:217], off
	s_waitcnt vmcnt(8)
	s_waitcnt lgkmcnt(0)
	s_barrier
	s_setprio 1
	s_waitcnt lgkmcnt(0)
	v_mfma_f32_16x16x128_f8f6f4 v[156:159], v[24:31], v[192:199], v[156:159]
	v_mfma_f32_16x16x128_f8f6f4 v[152:155], v[16:23], v[192:199], v[152:155]
	v_mfma_f32_16x16x128_f8f6f4 v[140:143], v[24:31], v[200:207], v[140:143]
	v_mfma_f32_16x16x128_f8f6f4 v[136:139], v[16:23], v[200:207], v[136:139]
	v_mfma_f32_16x16x128_f8f6f4 v[124:127], v[24:31], v[208:215], v[124:127]
	v_mfma_f32_16x16x128_f8f6f4 v[120:123], v[16:23], v[208:215], v[120:123]
	v_mfma_f32_16x16x128_f8f6f4 v[108:111], v[24:31], v[224:231], v[108:111]
	v_mfma_f32_16x16x128_f8f6f4 v[104:107], v[16:23], v[224:231], v[104:107]
	s_setprio 0
	s_setprio 1
	v_mfma_f32_16x16x128_f8f6f4 v[148:151], v[8:15], v[192:199], v[148:151]
	v_mfma_f32_16x16x128_f8f6f4 v[144:147], v[0:7], v[192:199], v[144:147]
	v_mfma_f32_16x16x128_f8f6f4 v[132:135], v[8:15], v[200:207], v[132:135]
	v_mfma_f32_16x16x128_f8f6f4 v[128:131], v[0:7], v[200:207], v[128:131]
	v_mfma_f32_16x16x128_f8f6f4 v[116:119], v[8:15], v[208:215], v[116:119]
	v_mfma_f32_16x16x128_f8f6f4 v[112:115], v[0:7], v[208:215], v[112:115]
	v_mfma_f32_16x16x128_f8f6f4 v[100:103], v[8:15], v[224:231], v[100:103]
	v_mfma_f32_16x16x128_f8f6f4 v[96:99], v[0:7], v[224:231], v[96:99]
	s_setprio 0
	s_barrier
	s_cmp_lt_u32 s21, 5
	s_cselect_b64 s[36:37], -1, 0
	s_and_b64 s[64:65], s[36:37], exec
	s_cselect_b32 s0, 0, -8
	s_cselect_b32 s67, s39, s35
	s_cselect_b32 s66, s38, s34
	s_add_i32 s0, s0, s21
	s_add_i32 s0, s0, 3
	s_lshl_b64 s[64:65], s[0:1], 7
	s_add_u32 s66, s66, s64
	s_addc_u32 s67, s67, s65
	s_add_i32 s0, s63, s48
	v_lshl_add_u64 v[216:217], s[66:67], 0, v[162:163]
	s_mov_b32 m0, s0
	ds_read_b128 v[192:195], v189 offset:49152
	ds_read_b128 v[196:199], v189 offset:50176
	ds_read_b128 v[200:203], v189 offset:51200
	ds_read_b128 v[204:207], v189 offset:52224
	ds_read_b128 v[208:211], v189 offset:53248
	ds_read_b128 v[212:215], v189 offset:54272
	ds_read_b128 v[224:227], v189 offset:55296
	ds_read_b128 v[228:231], v189 offset:56320
	global_load_lds_dwordx4 v[216:217], off
	s_add_i32 m0, s0, 0x2000
	v_lshl_add_u64 v[216:217], s[66:67], 0, v[166:167]
	s_add_u32 s66, s66, 0x20000
	s_addc_u32 s67, s67, 0
	s_add_i32 s0, s68, s48
	global_load_lds_dwordx4 v[216:217], off
	v_lshl_add_u64 v[216:217], s[66:67], 0, v[162:163]
	s_mov_b32 m0, s0
	s_nop 0
	global_load_lds_dwordx4 v[216:217], off
	s_add_i32 m0, s0, 0x2000
	s_and_b64 s[36:37], s[36:37], exec
	s_cselect_b32 s21, s40, s30
	s_cselect_b32 s0, s41, s31
	s_add_u32 s36, s21, s64
	v_lshl_add_u64 v[216:217], s[66:67], 0, v[166:167]
	s_addc_u32 s37, s0, s65
	global_load_lds_dwordx4 v[216:217], off
	v_lshl_add_u64 v[216:217], s[36:37], 0, v[160:161]
	s_mov_b32 m0, s57
	s_nop 0
	global_load_lds_dwordx4 v[216:217], off
	v_lshl_add_u64 v[216:217], s[36:37], 0, v[164:165]
	s_mov_b32 m0, s58
	s_nop 0
	global_load_lds_dwordx4 v[216:217], off
	s_waitcnt vmcnt(8)
	s_waitcnt lgkmcnt(0)
	s_barrier
	s_setprio 1
	s_waitcnt lgkmcnt(0)
	v_mfma_f32_16x16x128_f8f6f4 v[92:95], v[24:31], v[192:199], v[92:95]
	v_mfma_f32_16x16x128_f8f6f4 v[88:91], v[16:23], v[192:199], v[88:91]
	v_mfma_f32_16x16x128_f8f6f4 v[76:79], v[24:31], v[200:207], v[76:79]
	v_mfma_f32_16x16x128_f8f6f4 v[72:75], v[16:23], v[200:207], v[72:75]
	v_mfma_f32_16x16x128_f8f6f4 v[56:59], v[24:31], v[208:215], v[56:59]
	v_mfma_f32_16x16x128_f8f6f4 v[48:51], v[16:23], v[208:215], v[48:51]
	v_mfma_f32_16x16x128_f8f6f4 v[36:39], v[24:31], v[224:231], v[36:39]
	v_mfma_f32_16x16x128_f8f6f4 v[32:35], v[16:23], v[224:231], v[32:35]
	s_setprio 0
	s_setprio 1
	v_mfma_f32_16x16x128_f8f6f4 v[84:87], v[8:15], v[192:199], v[84:87]
	v_mfma_f32_16x16x128_f8f6f4 v[80:83], v[0:7], v[192:199], v[80:83]
	v_mfma_f32_16x16x128_f8f6f4 v[68:71], v[8:15], v[200:207], v[68:71]
	v_mfma_f32_16x16x128_f8f6f4 v[64:67], v[0:7], v[200:207], v[64:67]
	v_mfma_f32_16x16x128_f8f6f4 v[60:63], v[8:15], v[208:215], v[60:63]
	v_mfma_f32_16x16x128_f8f6f4 v[52:55], v[0:7], v[208:215], v[52:55]
	v_mfma_f32_16x16x128_f8f6f4 v[44:47], v[8:15], v[224:231], v[44:47]
	v_mfma_f32_16x16x128_f8f6f4 v[40:43], v[0:7], v[224:231], v[40:43]
	s_setprio 0
	s_barrier
	v_lshl_add_u64 v[178:179], v[178:179], 0, s[16:17]
	v_lshl_add_u64 v[180:181], v[180:181], 0, s[16:17]
	s_mov_b32 s21, s23
	s_cbranch_vccnz .LBB0_959
	s_andn2_b64 vcc, exec, s[14:15]
	s_cbranch_vccnz .LBB0_962
	s_barrier

.LBB0_1182:
	v_add_u32_e32 v0, s69, v222
	v_add_u32_e32 v4, s70, v222
	ds_read_b128 v[24:27], v0
	ds_read_b128 v[28:31], v0 offset:1024
	ds_read_b128 v[16:19], v0 offset:2048
	ds_read_b128 v[20:23], v0 offset:3072
	ds_read_b128 v[8:11], v4
	ds_read_b128 v[12:15], v4 offset:1024
	ds_read_b128 v[0:3], v4 offset:2048
	ds_read_b128 v[4:7], v4 offset:3072
	v_lshl_add_u64 v[214:215], s[34:35], 0, v[192:193]
	s_add_i32 m0, s29, 0xc000
	ds_read_b128 v[32:35], v226
	ds_read_b128 v[36:39], v226 offset:1024
	ds_read_b128 v[40:43], v226 offset:2048
	ds_read_b128 v[44:47], v226 offset:3072
	ds_read_b128 v[48:51], v226 offset:4096
	ds_read_b128 v[52:55], v226 offset:5120
	ds_read_b128 v[56:59], v226 offset:6144
	ds_read_b128 v[60:63], v226 offset:7168
	global_load_lds_dwordx4 v[214:215], off
	v_lshl_add_u64 v[214:215], s[34:35], 0, v[210:211]
	s_add_i32 m0, s29, 0xe000
	s_nop 0
	global_load_lds_dwordx4 v[214:215], off
	s_waitcnt vmcnt(8)
	s_waitcnt lgkmcnt(0)
	s_barrier
	s_setprio 1
	s_waitcnt lgkmcnt(0)
	v_mfma_f32_16x16x128_f8f6f4 v[188:191], v[24:31], v[32:39], v[188:191]
	v_mfma_f32_16x16x128_f8f6f4 v[180:183], v[16:23], v[32:39], v[180:183]
	v_mfma_f32_16x16x128_f8f6f4 v[172:175], v[24:31], v[40:47], v[172:175]
	v_mfma_f32_16x16x128_f8f6f4 v[164:167], v[16:23], v[40:47], v[164:167]
	v_mfma_f32_16x16x128_f8f6f4 v[156:159], v[24:31], v[48:55], v[156:159]
	v_mfma_f32_16x16x128_f8f6f4 v[148:151], v[16:23], v[48:55], v[148:151]
	v_mfma_f32_16x16x128_f8f6f4 v[140:143], v[24:31], v[56:63], v[140:143]
	v_mfma_f32_16x16x128_f8f6f4 v[132:135], v[16:23], v[56:63], v[132:135]
	s_setprio 0
	s_setprio 1
	v_mfma_f32_16x16x128_f8f6f4 v[184:187], v[8:15], v[32:39], v[184:187]
	v_mfma_f32_16x16x128_f8f6f4 v[176:179], v[0:7], v[32:39], v[176:179]
	v_mfma_f32_16x16x128_f8f6f4 v[168:171], v[8:15], v[40:47], v[168:171]
	v_mfma_f32_16x16x128_f8f6f4 v[160:163], v[0:7], v[40:47], v[160:163]
	v_mfma_f32_16x16x128_f8f6f4 v[152:155], v[8:15], v[48:55], v[152:155]
	v_mfma_f32_16x16x128_f8f6f4 v[144:147], v[0:7], v[48:55], v[144:147]
	v_mfma_f32_16x16x128_f8f6f4 v[136:139], v[8:15], v[56:63], v[136:139]
	v_mfma_f32_16x16x128_f8f6f4 v[128:131], v[0:7], v[56:63], v[128:131]
	s_setprio 0
	s_barrier
	s_cmp_gt_u32 s25, 5
	v_sub_co_u32_e64 v216, s[40:41], s25, 6
	s_cselect_b64 vcc, -1, 0
	v_add_u32_e32 v217, 8, v216
	v_cndmask_b32_e32 v216, v217, v216, vcc
	v_ashrrev_i32_e32 v217, 31, v216
	v_cndmask_b32_e32 v215, v213, v205, vcc
	v_cndmask_b32_e32 v214, v212, v204, vcc
	v_lshlrev_b64 v[216:217], 7, v[216:217]
	v_lshl_add_u64 v[214:215], v[214:215], 0, v[216:217]
	s_add_i32 s26, s69, s7
	s_add_i32 s38, s26, 0x2000
	v_lshl_add_u64 v[236:237], v[214:215], 0, v[194:195]
	s_mov_b32 m0, s26
	ds_read_b128 v[56:59], v226 offset:16384
	ds_read_b128 v[60:63], v226 offset:17408
	ds_read_b128 v[48:51], v226 offset:18432
	ds_read_b128 v[52:55], v226 offset:19456
	ds_read_b128 v[40:43], v226 offset:20480
	ds_read_b128 v[44:47], v226 offset:21504
	ds_read_b128 v[32:35], v226 offset:22528
	ds_read_b128 v[36:39], v226 offset:23552
	v_lshl_add_u64 v[234:235], v[214:215], 0, s[0:1]
	s_add_i32 s39, s70, s7
	global_load_lds_dwordx4 v[236:237], off
	v_lshl_add_u64 v[214:215], v[214:215], 0, v[196:197]
	s_mov_b32 m0, s38
	s_add_i32 s42, s39, 0x2000
	global_load_lds_dwordx4 v[214:215], off
	v_lshl_add_u64 v[214:215], v[234:235], 0, v[194:195]
	s_mov_b32 m0, s39
	v_lshl_add_u64 v[216:217], s[8:9], 0, v[216:217]
	global_load_lds_dwordx4 v[214:215], off
	v_lshl_add_u64 v[214:215], v[234:235], 0, v[196:197]
	s_mov_b32 m0, s42
	v_readfirstlane_b32 s44, v216
	global_load_lds_dwordx4 v[214:215], off
	v_cndmask_b32_e32 v214, v206, v229, vcc
	v_readfirstlane_b32 s45, v217
	s_mov_b32 m0, s29
	v_cndmask_b32_e32 v215, v208, v230, vcc
	s_add_i32 s85, 0, 0x18000
	s_add_i32 s82, 0, 0x1c000
	s_cmp_gt_u32 s25, 4
	global_load_lds_dwordx4 v214, s[44:45]
	s_mov_b32 m0, s56
	s_cselect_b64 s[38:39], -1, 0
	global_load_lds_dwordx4 v215, s[44:45]
	s_and_b64 s[42:43], s[38:39], exec
	s_cselect_b32 s26, -5, 3
	s_add_i32 s42, s26, s25
	s_ashr_i32 s43, s42, 31
	s_add_i32 s84, s85, s7
	s_add_i32 s26, s82, s7
	v_cndmask_b32_e64 v215, v213, v205, s[38:39]
	v_cndmask_b32_e64 v214, v212, v204, s[38:39]
	s_lshl_b64 s[42:43], s[42:43], 7
	s_add_i32 s83, s84, 0x2000
	s_add_i32 s60, s26, 0x2000
	v_lshl_add_u64 v[216:217], v[214:215], 0, s[42:43]
	s_add_u32 s42, s8, s42
	s_waitcnt vmcnt(8)
	s_addc_u32 s43, s9, s43
	s_waitcnt lgkmcnt(0)
	s_add_u32 s34, s34, 0x100
	s_addc_u32 s35, s35, 0
	s_add_i32 s25, s25, 2
	v_lshl_add_u64 v[214:215], v[216:217], 0, s[0:1]
	s_barrier
	s_setprio 1
	s_waitcnt lgkmcnt(0)
	v_mfma_f32_16x16x128_f8f6f4 v[116:119], v[24:31], v[56:63], v[116:119]
	v_mfma_f32_16x16x128_f8f6f4 v[108:111], v[16:23], v[56:63], v[108:111]
	v_mfma_f32_16x16x128_f8f6f4 v[104:107], v[24:31], v[48:55], v[104:107]
	v_mfma_f32_16x16x128_f8f6f4 v[96:99], v[16:23], v[48:55], v[96:99]
	v_mfma_f32_16x16x128_f8f6f4 v[88:91], v[24:31], v[40:47], v[88:91]
	v_mfma_f32_16x16x128_f8f6f4 v[80:83], v[16:23], v[40:47], v[80:83]
	v_mfma_f32_16x16x128_f8f6f4 v[72:75], v[24:31], v[32:39], v[72:75]
	v_mfma_f32_16x16x128_f8f6f4 v[64:67], v[16:23], v[32:39], v[64:67]
	s_setprio 0
	s_setprio 1
	v_mfma_f32_16x16x128_f8f6f4 v[124:127], v[8:15], v[56:63], v[124:127]
	v_mfma_f32_16x16x128_f8f6f4 v[120:123], v[0:7], v[56:63], v[120:123]
	v_mfma_f32_16x16x128_f8f6f4 v[112:115], v[8:15], v[48:55], v[112:115]
	v_mfma_f32_16x16x128_f8f6f4 v[100:103], v[0:7], v[48:55], v[100:103]
	v_mfma_f32_16x16x128_f8f6f4 v[92:95], v[8:15], v[40:47], v[92:95]
	v_mfma_f32_16x16x128_f8f6f4 v[84:87], v[0:7], v[40:47], v[84:87]
	v_mfma_f32_16x16x128_f8f6f4 v[76:79], v[8:15], v[32:39], v[76:79]
	v_mfma_f32_16x16x128_f8f6f4 v[68:71], v[0:7], v[32:39], v[68:71]
	s_setprio 0
	s_barrier
	v_add_u32_e32 v12, s85, v222
	v_add_u32_e32 v28, s82, v222
	ds_read_b128 v[0:3], v12
	ds_read_b128 v[4:7], v12 offset:1024
	ds_read_b128 v[8:11], v12 offset:2048
	ds_read_b128 v[12:15], v12 offset:3072
	ds_read_b128 v[16:19], v28
	ds_read_b128 v[20:23], v28 offset:1024
	ds_read_b128 v[24:27], v28 offset:2048
	ds_read_b128 v[28:31], v28 offset:3072
	s_mov_b32 m0, s57
	v_cndmask_b32_e32 v223, v192, v231, vcc
	ds_read_b128 v[32:35], v226 offset:32768
	ds_read_b128 v[36:39], v226 offset:33792
	ds_read_b128 v[40:43], v226 offset:34816
	ds_read_b128 v[44:47], v226 offset:35840
	ds_read_b128 v[48:51], v226 offset:36864
	ds_read_b128 v[52:55], v226 offset:37888
	ds_read_b128 v[56:59], v226 offset:38912
	ds_read_b128 v[60:63], v226 offset:39936
	v_cndmask_b32_e32 v233, v210, v232, vcc
	global_load_lds_dwordx4 v223, s[44:45]
	s_mov_b32 m0, s58
	s_nop 0
	global_load_lds_dwordx4 v233, s[44:45]
	s_waitcnt vmcnt(8)
	s_waitcnt lgkmcnt(0)
	s_barrier
	s_setprio 1
	s_waitcnt lgkmcnt(0)
	v_mfma_f32_16x16x128_f8f6f4 v[188:191], v[0:7], v[32:39], v[188:191]
	v_mfma_f32_16x16x128_f8f6f4 v[180:183], v[8:15], v[32:39], v[180:183]
	v_mfma_f32_16x16x128_f8f6f4 v[172:175], v[0:7], v[40:47], v[172:175]
	v_mfma_f32_16x16x128_f8f6f4 v[164:167], v[8:15], v[40:47], v[164:167]
	v_mfma_f32_16x16x128_f8f6f4 v[156:159], v[0:7], v[48:55], v[156:159]
	v_mfma_f32_16x16x128_f8f6f4 v[148:151], v[8:15], v[48:55], v[148:151]
	v_mfma_f32_16x16x128_f8f6f4 v[140:143], v[0:7], v[56:63], v[140:143]
	v_mfma_f32_16x16x128_f8f6f4 v[132:135], v[8:15], v[56:63], v[132:135]
	s_setprio 0
	s_setprio 1
	v_mfma_f32_16x16x128_f8f6f4 v[184:187], v[16:23], v[32:39], v[184:187]
	v_mfma_f32_16x16x128_f8f6f4 v[176:179], v[24:31], v[32:39], v[176:179]
	v_mfma_f32_16x16x128_f8f6f4 v[168:171], v[16:23], v[40:47], v[168:171]
	v_mfma_f32_16x16x128_f8f6f4 v[160:163], v[24:31], v[40:47], v[160:163]
	v_mfma_f32_16x16x128_f8f6f4 v[152:155], v[16:23], v[48:55], v[152:155]
	v_mfma_f32_16x16x128_f8f6f4 v[144:147], v[24:31], v[48:55], v[144:147]
	v_mfma_f32_16x16x128_f8f6f4 v[136:139], v[16:23], v[56:63], v[136:139]
	v_mfma_f32_16x16x128_f8f6f4 v[128:131], v[24:31], v[56:63], v[128:131]
	s_setprio 0
	s_barrier
	s_mov_b32 m0, s84
	v_lshl_add_u64 v[234:235], v[216:217], 0, v[194:195]
	ds_read_b128 v[32:35], v226 offset:49152
	ds_read_b128 v[36:39], v226 offset:50176
	ds_read_b128 v[40:43], v226 offset:51200
	ds_read_b128 v[44:47], v226 offset:52224
	ds_read_b128 v[48:51], v226 offset:53248
	ds_read_b128 v[52:55], v226 offset:54272
	ds_read_b128 v[56:59], v226 offset:55296
	ds_read_b128 v[60:63], v226 offset:56320
	global_load_lds_dwordx4 v[234:235], off
	v_lshl_add_u64 v[216:217], v[216:217], 0, v[196:197]
	s_mov_b32 m0, s83
	s_nop 0
	global_load_lds_dwordx4 v[216:217], off
	v_lshl_add_u64 v[216:217], v[214:215], 0, v[194:195]
	s_mov_b32 m0, s26
	v_lshl_add_u64 v[214:215], v[214:215], 0, v[196:197]
	global_load_lds_dwordx4 v[216:217], off
	s_mov_b32 m0, s60
	s_nop 0
	global_load_lds_dwordx4 v[214:215], off
	v_cndmask_b32_e64 v214, v206, v229, s[38:39]
	s_mov_b32 m0, s59
	v_cndmask_b32_e64 v215, v208, v230, s[38:39]
	global_load_lds_dwordx4 v214, s[42:43]
	s_mov_b32 m0, s61
	s_nop 0
	global_load_lds_dwordx4 v215, s[42:43]
	s_waitcnt vmcnt(8)
	s_waitcnt lgkmcnt(0)
	s_barrier
	s_setprio 1
	s_waitcnt lgkmcnt(0)
	v_mfma_f32_16x16x128_f8f6f4 v[116:119], v[0:7], v[32:39], v[116:119]
	v_mfma_f32_16x16x128_f8f6f4 v[108:111], v[8:15], v[32:39], v[108:111]
	v_mfma_f32_16x16x128_f8f6f4 v[104:107], v[0:7], v[40:47], v[104:107]
	v_mfma_f32_16x16x128_f8f6f4 v[96:99], v[8:15], v[40:47], v[96:99]
	v_mfma_f32_16x16x128_f8f6f4 v[88:91], v[0:7], v[48:55], v[88:91]
	v_mfma_f32_16x16x128_f8f6f4 v[80:83], v[8:15], v[48:55], v[80:83]
	v_mfma_f32_16x16x128_f8f6f4 v[72:75], v[0:7], v[56:63], v[72:75]
	v_mfma_f32_16x16x128_f8f6f4 v[64:67], v[8:15], v[56:63], v[64:67]
	s_setprio 0
	s_setprio 1
	v_mfma_f32_16x16x128_f8f6f4 v[124:127], v[16:23], v[32:39], v[124:127]
	v_mfma_f32_16x16x128_f8f6f4 v[120:123], v[24:31], v[32:39], v[120:123]
	v_mfma_f32_16x16x128_f8f6f4 v[112:115], v[16:23], v[40:47], v[112:115]
	v_mfma_f32_16x16x128_f8f6f4 v[100:103], v[24:31], v[40:47], v[100:103]
	v_mfma_f32_16x16x128_f8f6f4 v[92:95], v[16:23], v[48:55], v[92:95]
	v_mfma_f32_16x16x128_f8f6f4 v[84:87], v[24:31], v[48:55], v[84:87]
	v_mfma_f32_16x16x128_f8f6f4 v[76:79], v[16:23], v[56:63], v[76:79]
	v_mfma_f32_16x16x128_f8f6f4 v[68:71], v[24:31], v[56:63], v[68:71]
	s_setprio 0
	s_barrier
	s_andn2_b64 vcc, exec, s[40:41]
	s_cbranch_vccnz .LBB0_1185

.LBB0_1263:
	ds_read_b128 v[24:27], v231
	ds_read_b128 v[28:31], v231 offset:1024
	ds_read_b128 v[16:19], v231 offset:2048
	ds_read_b128 v[20:23], v231 offset:3072
	ds_read_b128 v[8:11], v237
	ds_read_b128 v[12:15], v237 offset:1024
	ds_read_b128 v[0:3], v237 offset:2048
	ds_read_b128 v[4:7], v237 offset:3072
	s_add_i32 m0, s68, 0xc000
	ds_read_b128 v[166:169], v243
	ds_read_b128 v[170:173], v243 offset:1024
	ds_read_b128 v[174:177], v243 offset:2048
	ds_read_b128 v[178:181], v243 offset:3072
	ds_read_b128 v[182:185], v243 offset:4096
	ds_read_b128 v[186:189], v243 offset:5120
	ds_read_b128 v[216:219], v243 offset:6144
	ds_read_b128 v[220:223], v243 offset:7168
	global_load_lds_dwordx4 v[162:163], off
	s_add_i32 m0, s68, 0xe000
	s_nop 0
	global_load_lds_dwordx4 v[164:165], off
	s_waitcnt vmcnt(8)
	s_waitcnt lgkmcnt(0)
	s_barrier
	s_setprio 1
	s_waitcnt lgkmcnt(0)
	v_mfma_f32_16x16x128_f8f6f4 v[156:159], v[24:31], v[166:173], v[156:159]
	v_mfma_f32_16x16x128_f8f6f4 v[152:155], v[16:23], v[166:173], v[152:155]
	v_mfma_f32_16x16x128_f8f6f4 v[140:143], v[24:31], v[174:181], v[140:143]
	v_mfma_f32_16x16x128_f8f6f4 v[136:139], v[16:23], v[174:181], v[136:139]
	v_mfma_f32_16x16x128_f8f6f4 v[124:127], v[24:31], v[182:189], v[124:127]
	v_mfma_f32_16x16x128_f8f6f4 v[120:123], v[16:23], v[182:189], v[120:123]
	v_mfma_f32_16x16x128_f8f6f4 v[108:111], v[24:31], v[216:223], v[108:111]
	v_mfma_f32_16x16x128_f8f6f4 v[104:107], v[16:23], v[216:223], v[104:107]
	s_setprio 0
	s_setprio 1
	v_mfma_f32_16x16x128_f8f6f4 v[148:151], v[8:15], v[166:173], v[148:151]
	v_mfma_f32_16x16x128_f8f6f4 v[144:147], v[0:7], v[166:173], v[144:147]
	v_mfma_f32_16x16x128_f8f6f4 v[132:135], v[8:15], v[174:181], v[132:135]
	v_mfma_f32_16x16x128_f8f6f4 v[128:131], v[0:7], v[174:181], v[128:131]
	v_mfma_f32_16x16x128_f8f6f4 v[116:119], v[8:15], v[182:189], v[116:119]
	v_mfma_f32_16x16x128_f8f6f4 v[112:115], v[0:7], v[182:189], v[112:115]
	v_mfma_f32_16x16x128_f8f6f4 v[100:103], v[8:15], v[216:223], v[100:103]
	v_mfma_f32_16x16x128_f8f6f4 v[96:99], v[0:7], v[216:223], v[96:99]
	s_setprio 0
	s_barrier
	s_cmp_gt_u32 s43, 25
	v_sub_co_u32_e64 v200, s[40:41], s43, 26
	s_cselect_b64 vcc, -1, 0
	v_add_u32_e32 v210, 28, v200
	v_cndmask_b32_e32 v224, v210, v200, vcc
	v_ashrrev_i32_e32 v225, 31, v224
	v_cndmask_b32_e32 v191, v161, v209, vcc
	v_cndmask_b32_e32 v190, v160, v208, vcc
	v_lshlrev_b64 v[224:225], 7, v[224:225]
	v_lshl_add_u64 v[190:191], v[190:191], 0, v[224:225]
	s_add_i32 s44, s24, s66
	v_lshl_add_u64 v[228:229], v[190:191], 0, v[194:195]
	s_mov_b32 m0, s44
	ds_read_b128 v[166:169], v243 offset:16384
	ds_read_b128 v[170:173], v243 offset:17408
	ds_read_b128 v[174:177], v243 offset:18432
	ds_read_b128 v[178:181], v243 offset:19456
	ds_read_b128 v[182:185], v243 offset:20480
	ds_read_b128 v[186:189], v243 offset:21504
	ds_read_b128 v[216:219], v243 offset:22528
	ds_read_b128 v[220:223], v243 offset:23552
	global_load_lds_dwordx4 v[228:229], off
	v_lshl_add_u64 v[228:229], v[190:191], 0, v[198:199]
	s_add_i32 m0, s44, 0x2000
	v_lshl_add_u64 v[190:191], v[190:191], 0, s[0:1]
	s_add_i32 s44, s80, s66
	global_load_lds_dwordx4 v[228:229], off
	v_lshl_add_u64 v[228:229], v[190:191], 0, v[194:195]
	s_mov_b32 m0, s44
	v_lshl_add_u64 v[190:191], v[190:191], 0, v[198:199]
	global_load_lds_dwordx4 v[228:229], off
	s_add_i32 m0, s44, 0x2000
	s_and_b64 s[44:45], vcc, exec
	s_cselect_b32 s45, s63, s39
	s_cselect_b32 s44, s62, s38
	global_load_lds_dwordx4 v[190:191], off
	v_lshl_add_u64 v[190:191], s[44:45], 0, v[224:225]
	v_lshl_add_u64 v[224:225], v[190:191], 0, v[192:193]
	s_mov_b32 m0, s68
	s_nop 0
	global_load_lds_dwordx4 v[224:225], off
	v_lshl_add_u64 v[224:225], v[190:191], 0, v[196:197]
	s_mov_b32 m0, s69
	s_nop 0
	global_load_lds_dwordx4 v[224:225], off
	s_waitcnt vmcnt(8)
	s_waitcnt lgkmcnt(0)
	s_barrier
	s_setprio 1
	s_waitcnt lgkmcnt(0)
	v_mfma_f32_16x16x128_f8f6f4 v[92:95], v[24:31], v[166:173], v[92:95]
	v_mfma_f32_16x16x128_f8f6f4 v[88:91], v[16:23], v[166:173], v[88:91]
	v_mfma_f32_16x16x128_f8f6f4 v[76:79], v[24:31], v[174:181], v[76:79]
	v_mfma_f32_16x16x128_f8f6f4 v[72:75], v[16:23], v[174:181], v[72:75]
	v_mfma_f32_16x16x128_f8f6f4 v[52:55], v[24:31], v[182:189], v[52:55]
	v_mfma_f32_16x16x128_f8f6f4 v[48:51], v[16:23], v[182:189], v[48:51]
	v_mfma_f32_16x16x128_f8f6f4 v[36:39], v[24:31], v[216:223], v[36:39]
	v_mfma_f32_16x16x128_f8f6f4 v[32:35], v[16:23], v[216:223], v[32:35]
	s_setprio 0
	s_setprio 1
	v_mfma_f32_16x16x128_f8f6f4 v[84:87], v[8:15], v[166:173], v[84:87]
	v_mfma_f32_16x16x128_f8f6f4 v[80:83], v[0:7], v[166:173], v[80:83]
	v_mfma_f32_16x16x128_f8f6f4 v[60:63], v[8:15], v[174:181], v[60:63]
	v_mfma_f32_16x16x128_f8f6f4 v[56:59], v[0:7], v[174:181], v[56:59]
	v_mfma_f32_16x16x128_f8f6f4 v[68:71], v[8:15], v[182:189], v[68:71]
	v_mfma_f32_16x16x128_f8f6f4 v[64:67], v[0:7], v[182:189], v[64:67]
	v_mfma_f32_16x16x128_f8f6f4 v[44:47], v[8:15], v[216:223], v[44:47]
	v_mfma_f32_16x16x128_f8f6f4 v[40:43], v[0:7], v[216:223], v[40:43]
	s_setprio 0
	s_barrier
	s_add_i32 s46, 0, 0x18000
	s_add_i32 s47, 0, 0x1c000
	v_add_u32_e32 v0, s46, v215
	v_add_u32_e32 v4, s47, v215
	ds_read_b128 v[16:19], v0
	ds_read_b128 v[20:23], v0 offset:1024
	ds_read_b128 v[24:27], v0 offset:2048
	ds_read_b128 v[28:31], v0 offset:3072
	ds_read_b128 v[8:11], v4
	ds_read_b128 v[12:15], v4 offset:1024
	ds_read_b128 v[0:3], v4 offset:2048
	ds_read_b128 v[4:7], v4 offset:3072
	v_lshl_add_u64 v[190:191], v[190:191], 0, s[0:1]
	s_mov_b32 m0, s70
	v_lshl_add_u64 v[224:225], v[190:191], 0, v[192:193]
	ds_read_b128 v[166:169], v243 offset:32768
	ds_read_b128 v[170:173], v243 offset:33792
	ds_read_b128 v[174:177], v243 offset:34816
	ds_read_b128 v[178:181], v243 offset:35840
	ds_read_b128 v[182:185], v243 offset:36864
	ds_read_b128 v[186:189], v243 offset:37888
	ds_read_b128 v[216:219], v243 offset:38912
	ds_read_b128 v[220:223], v243 offset:39936
	global_load_lds_dwordx4 v[224:225], off
	v_lshl_add_u64 v[190:191], v[190:191], 0, v[196:197]
	s_mov_b32 m0, s71
	s_nop 0
	global_load_lds_dwordx4 v[190:191], off
	s_waitcnt vmcnt(8)
	s_waitcnt lgkmcnt(0)
	s_barrier
	s_setprio 1
	s_waitcnt lgkmcnt(0)
	v_mfma_f32_16x16x128_f8f6f4 v[156:159], v[16:23], v[166:173], v[156:159]
	v_mfma_f32_16x16x128_f8f6f4 v[152:155], v[24:31], v[166:173], v[152:155]
	v_mfma_f32_16x16x128_f8f6f4 v[140:143], v[16:23], v[174:181], v[140:143]
	v_mfma_f32_16x16x128_f8f6f4 v[136:139], v[24:31], v[174:181], v[136:139]
	v_mfma_f32_16x16x128_f8f6f4 v[124:127], v[16:23], v[182:189], v[124:127]
	v_mfma_f32_16x16x128_f8f6f4 v[120:123], v[24:31], v[182:189], v[120:123]
	v_mfma_f32_16x16x128_f8f6f4 v[108:111], v[16:23], v[216:223], v[108:111]
	v_mfma_f32_16x16x128_f8f6f4 v[104:107], v[24:31], v[216:223], v[104:107]
	s_setprio 0
	s_setprio 1
	v_mfma_f32_16x16x128_f8f6f4 v[148:151], v[8:15], v[166:173], v[148:151]
	v_mfma_f32_16x16x128_f8f6f4 v[144:147], v[0:7], v[166:173], v[144:147]
	v_mfma_f32_16x16x128_f8f6f4 v[132:135], v[8:15], v[174:181], v[132:135]
	v_mfma_f32_16x16x128_f8f6f4 v[128:131], v[0:7], v[174:181], v[128:131]
	v_mfma_f32_16x16x128_f8f6f4 v[116:119], v[8:15], v[182:189], v[116:119]
	v_mfma_f32_16x16x128_f8f6f4 v[112:115], v[0:7], v[182:189], v[112:115]
	v_mfma_f32_16x16x128_f8f6f4 v[100:103], v[8:15], v[216:223], v[100:103]
	v_mfma_f32_16x16x128_f8f6f4 v[96:99], v[0:7], v[216:223], v[96:99]
	s_setprio 0
	s_barrier
	s_cmp_gt_u32 s43, 24
	s_cselect_b64 vcc, -1, 0
	s_and_b64 s[44:45], vcc, exec
	s_cselect_b32 s44, 0xffffffe7, 3
	s_add_i32 s44, s44, s43
	s_ashr_i32 s45, s44, 31
	v_cndmask_b32_e32 v191, v161, v209, vcc
	v_cndmask_b32_e32 v190, v160, v208, vcc
	s_lshl_b64 s[44:45], s[44:45], 7
	v_lshl_add_u64 v[190:191], v[190:191], 0, s[44:45]
	s_add_i32 s46, s46, s66
	v_lshl_add_u64 v[224:225], v[190:191], 0, v[194:195]
	s_mov_b32 m0, s46
	ds_read_b128 v[166:169], v243 offset:49152
	ds_read_b128 v[170:173], v243 offset:50176
	ds_read_b128 v[174:177], v243 offset:51200
	ds_read_b128 v[178:181], v243 offset:52224
	ds_read_b128 v[182:185], v243 offset:53248
	ds_read_b128 v[186:189], v243 offset:54272
	ds_read_b128 v[216:219], v243 offset:55296
	ds_read_b128 v[220:223], v243 offset:56320
	global_load_lds_dwordx4 v[224:225], off
	v_lshl_add_u64 v[224:225], v[190:191], 0, v[198:199]
	s_add_i32 m0, s46, 0x2000
	v_lshl_add_u64 v[190:191], v[190:191], 0, s[0:1]
	s_add_i32 s46, s47, s66
	global_load_lds_dwordx4 v[224:225], off
	v_lshl_add_u64 v[224:225], v[190:191], 0, v[194:195]
	s_mov_b32 m0, s46
	v_lshl_add_u64 v[190:191], v[190:191], 0, v[198:199]
	global_load_lds_dwordx4 v[224:225], off
	s_add_i32 m0, s46, 0x2000
	s_and_b64 s[46:47], vcc, exec
	s_cselect_b32 s47, s62, s38
	s_cselect_b32 s46, s63, s39
	s_add_u32 s44, s47, s44
	s_addc_u32 s45, s46, s45
	global_load_lds_dwordx4 v[190:191], off
	v_lshl_add_u64 v[190:191], s[44:45], 0, v[192:193]
	s_mov_b32 m0, s78
	s_nop 0
	global_load_lds_dwordx4 v[190:191], off
	v_lshl_add_u64 v[190:191], s[44:45], 0, v[196:197]
	s_mov_b32 m0, s79
	s_nop 0
	global_load_lds_dwordx4 v[190:191], off
	s_waitcnt vmcnt(8)
	s_waitcnt lgkmcnt(0)
	s_barrier
	s_setprio 1
	s_waitcnt lgkmcnt(0)
	v_mfma_f32_16x16x128_f8f6f4 v[92:95], v[16:23], v[166:173], v[92:95]
	v_mfma_f32_16x16x128_f8f6f4 v[88:91], v[24:31], v[166:173], v[88:91]
	v_mfma_f32_16x16x128_f8f6f4 v[76:79], v[16:23], v[174:181], v[76:79]
	v_mfma_f32_16x16x128_f8f6f4 v[72:75], v[24:31], v[174:181], v[72:75]
	v_mfma_f32_16x16x128_f8f6f4 v[52:55], v[16:23], v[182:189], v[52:55]
	v_mfma_f32_16x16x128_f8f6f4 v[48:51], v[24:31], v[182:189], v[48:51]
	v_mfma_f32_16x16x128_f8f6f4 v[36:39], v[16:23], v[216:223], v[36:39]
	v_mfma_f32_16x16x128_f8f6f4 v[32:35], v[24:31], v[216:223], v[32:35]
	s_setprio 0
	s_setprio 1
	v_mfma_f32_16x16x128_f8f6f4 v[84:87], v[8:15], v[166:173], v[84:87]
	v_mfma_f32_16x16x128_f8f6f4 v[80:83], v[0:7], v[166:173], v[80:83]
	v_mfma_f32_16x16x128_f8f6f4 v[60:63], v[8:15], v[174:181], v[60:63]
	v_mfma_f32_16x16x128_f8f6f4 v[56:59], v[0:7], v[174:181], v[56:59]
	v_mfma_f32_16x16x128_f8f6f4 v[68:71], v[8:15], v[182:189], v[68:71]
	v_mfma_f32_16x16x128_f8f6f4 v[64:67], v[0:7], v[182:189], v[64:67]
	v_mfma_f32_16x16x128_f8f6f4 v[44:47], v[8:15], v[216:223], v[44:47]
	v_mfma_f32_16x16x128_f8f6f4 v[40:43], v[0:7], v[216:223], v[40:43]
	s_setprio 0
	s_barrier
	v_lshl_add_u64 v[162:163], v[162:163], 0, s[34:35]
	v_lshl_add_u64 v[164:165], v[164:165], 0, s[34:35]
	s_add_i32 s43, s43, 2
	s_and_b64 vcc, exec, s[40:41]
	s_cbranch_vccnz .LBB0_1263
	s_andn2_b64 vcc, exec, s[30:31]
	s_cbranch_vccnz .LBB0_1266
	s_barrier

.LBB0_1292:
	v_add_u32_e32 v0, s78, v186
	v_add_u32_e32 v4, s79, v186
	ds_read_b128 v[24:27], v0
	ds_read_b128 v[28:31], v0 offset:1024
	ds_read_b128 v[16:19], v0 offset:2048
	ds_read_b128 v[20:23], v0 offset:3072
	ds_read_b128 v[8:11], v4
	ds_read_b128 v[12:15], v4 offset:1024
	ds_read_b128 v[0:3], v4 offset:2048
	ds_read_b128 v[4:7], v4 offset:3072
	v_lshl_add_u64 v[228:229], s[42:43], 0, v[160:161]
	s_add_i32 m0, s39, 0xc000
	ds_read_b128 v[196:199], v189
	ds_read_b128 v[200:203], v189 offset:1024
	ds_read_b128 v[204:207], v189 offset:2048
	ds_read_b128 v[208:211], v189 offset:3072
	ds_read_b128 v[212:215], v189 offset:4096
	ds_read_b128 v[216:219], v189 offset:5120
	ds_read_b128 v[220:223], v189 offset:6144
	ds_read_b128 v[224:227], v189 offset:7168
	global_load_lds_dwordx4 v[228:229], off
	v_lshl_add_u64 v[228:229], s[42:43], 0, v[178:179]
	s_add_i32 m0, s39, 0xe000
	s_nop 0
	global_load_lds_dwordx4 v[228:229], off
	s_waitcnt vmcnt(8)
	s_waitcnt lgkmcnt(0)
	s_barrier
	s_setprio 1
	s_waitcnt lgkmcnt(0)
	v_mfma_f32_16x16x128_f8f6f4 v[156:159], v[24:31], v[196:203], v[156:159]
	v_mfma_f32_16x16x128_f8f6f4 v[148:151], v[16:23], v[196:203], v[148:151]
	v_mfma_f32_16x16x128_f8f6f4 v[140:143], v[24:31], v[204:211], v[140:143]
	v_mfma_f32_16x16x128_f8f6f4 v[132:135], v[16:23], v[204:211], v[132:135]
	v_mfma_f32_16x16x128_f8f6f4 v[124:127], v[24:31], v[212:219], v[124:127]
	v_mfma_f32_16x16x128_f8f6f4 v[116:119], v[16:23], v[212:219], v[116:119]
	v_mfma_f32_16x16x128_f8f6f4 v[108:111], v[24:31], v[220:227], v[108:111]
	v_mfma_f32_16x16x128_f8f6f4 v[100:103], v[16:23], v[220:227], v[100:103]
	s_setprio 0
	s_setprio 1
	v_mfma_f32_16x16x128_f8f6f4 v[152:155], v[8:15], v[196:203], v[152:155]
	v_mfma_f32_16x16x128_f8f6f4 v[144:147], v[0:7], v[196:203], v[144:147]
	v_mfma_f32_16x16x128_f8f6f4 v[136:139], v[8:15], v[204:211], v[136:139]
	v_mfma_f32_16x16x128_f8f6f4 v[128:131], v[0:7], v[204:211], v[128:131]
	v_mfma_f32_16x16x128_f8f6f4 v[120:123], v[8:15], v[212:219], v[120:123]
	v_mfma_f32_16x16x128_f8f6f4 v[112:115], v[0:7], v[212:219], v[112:115]
	v_mfma_f32_16x16x128_f8f6f4 v[104:107], v[8:15], v[220:227], v[104:107]
	v_mfma_f32_16x16x128_f8f6f4 v[96:99], v[0:7], v[220:227], v[96:99]
	s_setprio 0
	s_barrier
	s_cmp_gt_u32 s31, 5
	v_sub_co_u32_e64 v230, s[44:45], s31, 6
	s_cselect_b64 vcc, -1, 0
	v_add_u32_e32 v231, 8, v230
	v_cndmask_b32_e32 v230, v231, v230, vcc
	v_ashrrev_i32_e32 v231, 31, v230
	v_cndmask_b32_e32 v229, v181, v173, vcc
	v_cndmask_b32_e32 v228, v180, v172, vcc
	v_lshlrev_b64 v[230:231], 7, v[230:231]
	v_lshl_add_u64 v[228:229], v[228:229], 0, v[230:231]
	s_add_i32 s34, s78, s7
	v_lshl_add_u64 v[232:233], v[228:229], 0, v[162:163]
	s_mov_b32 m0, s34
	ds_read_b128 v[196:199], v189 offset:16384
	ds_read_b128 v[200:203], v189 offset:17408
	ds_read_b128 v[204:207], v189 offset:18432
	ds_read_b128 v[208:211], v189 offset:19456
	ds_read_b128 v[212:215], v189 offset:20480
	ds_read_b128 v[216:219], v189 offset:21504
	ds_read_b128 v[220:223], v189 offset:22528
	ds_read_b128 v[224:227], v189 offset:23552
	global_load_lds_dwordx4 v[232:233], off
	v_lshl_add_u64 v[232:233], v[228:229], 0, v[164:165]
	s_add_i32 m0, s34, 0x2000
	v_lshl_add_u64 v[228:229], v[228:229], 0, s[22:23]
	s_add_i32 s34, s79, s7
	global_load_lds_dwordx4 v[232:233], off
	v_lshl_add_u64 v[232:233], v[228:229], 0, v[162:163]
	s_mov_b32 m0, s34
	v_lshl_add_u64 v[228:229], v[228:229], 0, v[164:165]
	global_load_lds_dwordx4 v[232:233], off
	s_add_i32 m0, s34, 0x2000
	s_nop 0
	global_load_lds_dwordx4 v[228:229], off
	v_lshl_add_u64 v[228:229], s[8:9], 0, v[230:231]
	v_cndmask_b32_e32 v230, v174, v192, vcc
	v_readfirstlane_b32 s46, v228
	v_readfirstlane_b32 s47, v229
	s_mov_b32 m0, s39
	v_cndmask_b32_e32 v231, v176, v193, vcc
	s_nop 2
	global_load_lds_dwordx4 v230, s[46:47]
	s_mov_b32 m0, s56
	s_nop 0
	global_load_lds_dwordx4 v231, s[46:47]
	s_waitcnt vmcnt(8)
	s_waitcnt lgkmcnt(0)
	s_barrier
	s_setprio 1
	s_waitcnt lgkmcnt(0)
	v_mfma_f32_16x16x128_f8f6f4 v[84:87], v[24:31], v[196:203], v[84:87]
	v_mfma_f32_16x16x128_f8f6f4 v[76:79], v[16:23], v[196:203], v[76:79]
	v_mfma_f32_16x16x128_f8f6f4 v[72:75], v[24:31], v[204:211], v[72:75]
	v_mfma_f32_16x16x128_f8f6f4 v[64:67], v[16:23], v[204:211], v[64:67]
	v_mfma_f32_16x16x128_f8f6f4 v[56:59], v[24:31], v[212:219], v[56:59]
	v_mfma_f32_16x16x128_f8f6f4 v[48:51], v[16:23], v[212:219], v[48:51]
	v_mfma_f32_16x16x128_f8f6f4 v[40:43], v[24:31], v[220:227], v[40:43]
	v_mfma_f32_16x16x128_f8f6f4 v[32:35], v[16:23], v[220:227], v[32:35]
	s_setprio 0
	s_setprio 1
	v_mfma_f32_16x16x128_f8f6f4 v[92:95], v[8:15], v[196:203], v[92:95]
	v_mfma_f32_16x16x128_f8f6f4 v[88:91], v[0:7], v[196:203], v[88:91]
	v_mfma_f32_16x16x128_f8f6f4 v[80:83], v[8:15], v[204:211], v[80:83]
	v_mfma_f32_16x16x128_f8f6f4 v[68:71], v[0:7], v[204:211], v[68:71]
	v_mfma_f32_16x16x128_f8f6f4 v[60:63], v[8:15], v[212:219], v[60:63]
	v_mfma_f32_16x16x128_f8f6f4 v[52:55], v[0:7], v[212:219], v[52:55]
	v_mfma_f32_16x16x128_f8f6f4 v[44:47], v[8:15], v[220:227], v[44:47]
	v_mfma_f32_16x16x128_f8f6f4 v[36:39], v[0:7], v[220:227], v[36:39]
	s_setprio 0
	s_barrier
	s_add_i32 s34, 0, 0x18000
	s_add_i32 s85, 0, 0x1c000
	v_add_u32_e32 v0, s34, v186
	v_add_u32_e32 v4, s85, v186
	ds_read_b128 v[16:19], v0
	ds_read_b128 v[20:23], v0 offset:1024
	ds_read_b128 v[24:27], v0 offset:2048
	ds_read_b128 v[28:31], v0 offset:3072
	ds_read_b128 v[8:11], v4
	ds_read_b128 v[12:15], v4 offset:1024
	ds_read_b128 v[0:3], v4 offset:2048
	ds_read_b128 v[4:7], v4 offset:3072
	s_mov_b32 m0, s57
	v_cndmask_b32_e32 v228, v160, v194, vcc
	ds_read_b128 v[196:199], v189 offset:32768
	ds_read_b128 v[200:203], v189 offset:33792
	ds_read_b128 v[204:207], v189 offset:34816
	ds_read_b128 v[208:211], v189 offset:35840
	ds_read_b128 v[212:215], v189 offset:36864
	ds_read_b128 v[216:219], v189 offset:37888
	ds_read_b128 v[220:223], v189 offset:38912
	ds_read_b128 v[224:227], v189 offset:39936
	v_cndmask_b32_e32 v229, v178, v195, vcc
	global_load_lds_dwordx4 v228, s[46:47]
	s_mov_b32 m0, s66
	s_nop 0
	global_load_lds_dwordx4 v229, s[46:47]
	s_waitcnt vmcnt(8)
	s_waitcnt lgkmcnt(0)
	s_barrier
	s_setprio 1
	s_waitcnt lgkmcnt(0)
	v_mfma_f32_16x16x128_f8f6f4 v[156:159], v[16:23], v[196:203], v[156:159]
	v_mfma_f32_16x16x128_f8f6f4 v[148:151], v[24:31], v[196:203], v[148:151]
	v_mfma_f32_16x16x128_f8f6f4 v[140:143], v[16:23], v[204:211], v[140:143]
	v_mfma_f32_16x16x128_f8f6f4 v[132:135], v[24:31], v[204:211], v[132:135]
	v_mfma_f32_16x16x128_f8f6f4 v[124:127], v[16:23], v[212:219], v[124:127]
	v_mfma_f32_16x16x128_f8f6f4 v[116:119], v[24:31], v[212:219], v[116:119]
	v_mfma_f32_16x16x128_f8f6f4 v[108:111], v[16:23], v[220:227], v[108:111]
	v_mfma_f32_16x16x128_f8f6f4 v[100:103], v[24:31], v[220:227], v[100:103]
	s_setprio 0
	s_setprio 1
	v_mfma_f32_16x16x128_f8f6f4 v[152:155], v[8:15], v[196:203], v[152:155]
	v_mfma_f32_16x16x128_f8f6f4 v[144:147], v[0:7], v[196:203], v[144:147]
	v_mfma_f32_16x16x128_f8f6f4 v[136:139], v[8:15], v[204:211], v[136:139]
	v_mfma_f32_16x16x128_f8f6f4 v[128:131], v[0:7], v[204:211], v[128:131]
	v_mfma_f32_16x16x128_f8f6f4 v[120:123], v[8:15], v[212:219], v[120:123]
	v_mfma_f32_16x16x128_f8f6f4 v[112:115], v[0:7], v[212:219], v[112:115]
	v_mfma_f32_16x16x128_f8f6f4 v[104:107], v[8:15], v[220:227], v[104:107]
	v_mfma_f32_16x16x128_f8f6f4 v[96:99], v[0:7], v[220:227], v[96:99]
	s_setprio 0
	s_barrier
	s_cmp_gt_u32 s31, 4
	s_cselect_b64 vcc, -1, 0
	s_and_b64 s[46:47], vcc, exec
	s_cselect_b32 s46, -5, 3
	s_add_i32 s46, s46, s31
	s_ashr_i32 s47, s46, 31
	v_cndmask_b32_e32 v229, v181, v173, vcc
	v_cndmask_b32_e32 v228, v180, v172, vcc
	s_lshl_b64 s[46:47], s[46:47], 7
	v_lshl_add_u64 v[228:229], v[228:229], 0, s[46:47]
	s_add_i32 s34, s34, s7
	v_lshl_add_u64 v[230:231], v[228:229], 0, v[162:163]
	s_mov_b32 m0, s34
	ds_read_b128 v[196:199], v189 offset:49152
	ds_read_b128 v[200:203], v189 offset:50176
	ds_read_b128 v[204:207], v189 offset:51200
	ds_read_b128 v[208:211], v189 offset:52224
	ds_read_b128 v[212:215], v189 offset:53248
	ds_read_b128 v[216:219], v189 offset:54272
	ds_read_b128 v[220:223], v189 offset:55296
	ds_read_b128 v[224:227], v189 offset:56320
	global_load_lds_dwordx4 v[230:231], off
	v_lshl_add_u64 v[230:231], v[228:229], 0, v[164:165]
	s_add_i32 m0, s34, 0x2000
	v_lshl_add_u64 v[228:229], v[228:229], 0, s[22:23]
	s_add_i32 s34, s85, s7
	global_load_lds_dwordx4 v[230:231], off
	v_lshl_add_u64 v[230:231], v[228:229], 0, v[162:163]
	s_mov_b32 m0, s34
	v_lshl_add_u64 v[228:229], v[228:229], 0, v[164:165]
	global_load_lds_dwordx4 v[230:231], off
	s_add_i32 m0, s34, 0x2000
	s_add_u32 s46, s8, s46
	global_load_lds_dwordx4 v[228:229], off
	s_addc_u32 s47, s9, s47
	v_cndmask_b32_e32 v228, v174, v192, vcc
	s_mov_b32 m0, s67
	v_cndmask_b32_e32 v229, v176, v193, vcc
	global_load_lds_dwordx4 v228, s[46:47]
	s_mov_b32 m0, s68
	s_nop 0
	global_load_lds_dwordx4 v229, s[46:47]
	s_waitcnt vmcnt(8)
	s_waitcnt lgkmcnt(0)
	s_barrier
	s_setprio 1
	s_waitcnt lgkmcnt(0)
	v_mfma_f32_16x16x128_f8f6f4 v[84:87], v[16:23], v[196:203], v[84:87]
	v_mfma_f32_16x16x128_f8f6f4 v[76:79], v[24:31], v[196:203], v[76:79]
	v_mfma_f32_16x16x128_f8f6f4 v[72:75], v[16:23], v[204:211], v[72:75]
	v_mfma_f32_16x16x128_f8f6f4 v[64:67], v[24:31], v[204:211], v[64:67]
	v_mfma_f32_16x16x128_f8f6f4 v[56:59], v[16:23], v[212:219], v[56:59]
	v_mfma_f32_16x16x128_f8f6f4 v[48:51], v[24:31], v[212:219], v[48:51]
	v_mfma_f32_16x16x128_f8f6f4 v[40:43], v[16:23], v[220:227], v[40:43]
	v_mfma_f32_16x16x128_f8f6f4 v[32:35], v[24:31], v[220:227], v[32:35]
	s_setprio 0
	s_setprio 1
	v_mfma_f32_16x16x128_f8f6f4 v[92:95], v[8:15], v[196:203], v[92:95]
	v_mfma_f32_16x16x128_f8f6f4 v[88:91], v[0:7], v[196:203], v[88:91]
	v_mfma_f32_16x16x128_f8f6f4 v[80:83], v[8:15], v[204:211], v[80:83]
	v_mfma_f32_16x16x128_f8f6f4 v[68:71], v[0:7], v[204:211], v[68:71]
	v_mfma_f32_16x16x128_f8f6f4 v[60:63], v[8:15], v[212:219], v[60:63]
	v_mfma_f32_16x16x128_f8f6f4 v[52:55], v[0:7], v[212:219], v[52:55]
	v_mfma_f32_16x16x128_f8f6f4 v[44:47], v[8:15], v[220:227], v[44:47]
	v_mfma_f32_16x16x128_f8f6f4 v[36:39], v[0:7], v[220:227], v[36:39]
	s_setprio 0
	s_barrier
	s_add_u32 s42, s42, 0x100
	s_addc_u32 s43, s43, 0
	s_add_i32 s31, s31, 2
	s_and_b64 vcc, exec, s[44:45]
	s_cbranch_vccz .LBB0_1295

.LBB0_1373:
	ds_read_b128 v[24:27], v217
	ds_read_b128 v[28:31], v217 offset:1024
	ds_read_b128 v[16:19], v217 offset:2048
	ds_read_b128 v[20:23], v217 offset:3072
	ds_read_b128 v[8:11], v221
	ds_read_b128 v[12:15], v221 offset:1024
	ds_read_b128 v[0:3], v221 offset:2048
	ds_read_b128 v[4:7], v221 offset:3072
	s_add_i32 m0, s70, 0xc000
	ds_read_b128 v[166:169], v225
	ds_read_b128 v[170:173], v225 offset:1024
	ds_read_b128 v[174:177], v225 offset:2048
	ds_read_b128 v[178:181], v225 offset:3072
	ds_read_b128 v[226:229], v225 offset:4096
	ds_read_b128 v[230:233], v225 offset:5120
	ds_read_b128 v[238:241], v225 offset:6144
	ds_read_b128 v[242:245], v225 offset:7168
	global_load_lds_dwordx4 v[162:163], off
	s_add_i32 m0, s70, 0xe000
	s_nop 0
	global_load_lds_dwordx4 v[164:165], off
	s_waitcnt vmcnt(8)
	s_waitcnt lgkmcnt(0)
	s_barrier
	s_setprio 1
	s_waitcnt lgkmcnt(0)
	v_mfma_f32_16x16x128_f8f6f4 v[156:159], v[24:31], v[166:173], v[156:159]
	v_mfma_f32_16x16x128_f8f6f4 v[152:155], v[16:23], v[166:173], v[152:155]
	v_mfma_f32_16x16x128_f8f6f4 v[140:143], v[24:31], v[174:181], v[140:143]
	v_mfma_f32_16x16x128_f8f6f4 v[136:139], v[16:23], v[174:181], v[136:139]
	v_mfma_f32_16x16x128_f8f6f4 v[124:127], v[24:31], v[226:233], v[124:127]
	v_mfma_f32_16x16x128_f8f6f4 v[120:123], v[16:23], v[226:233], v[120:123]
	v_mfma_f32_16x16x128_f8f6f4 v[108:111], v[24:31], v[238:245], v[108:111]
	v_mfma_f32_16x16x128_f8f6f4 v[104:107], v[16:23], v[238:245], v[104:107]
	s_setprio 0
	s_setprio 1
	v_mfma_f32_16x16x128_f8f6f4 v[148:151], v[8:15], v[166:173], v[148:151]
	v_mfma_f32_16x16x128_f8f6f4 v[144:147], v[0:7], v[166:173], v[144:147]
	v_mfma_f32_16x16x128_f8f6f4 v[132:135], v[8:15], v[174:181], v[132:135]
	v_mfma_f32_16x16x128_f8f6f4 v[128:131], v[0:7], v[174:181], v[128:131]
	v_mfma_f32_16x16x128_f8f6f4 v[116:119], v[8:15], v[226:233], v[116:119]
	v_mfma_f32_16x16x128_f8f6f4 v[112:115], v[0:7], v[226:233], v[112:115]
	v_mfma_f32_16x16x128_f8f6f4 v[100:103], v[8:15], v[238:245], v[100:103]
	v_mfma_f32_16x16x128_f8f6f4 v[96:99], v[0:7], v[238:245], v[96:99]
	s_setprio 0
	s_barrier
	s_cmp_gt_u32 s39, 25
	v_sub_co_u32_e64 v192, s[30:31], s39, 26
	s_cselect_b64 vcc, -1, 0
	v_add_u32_e32 v202, 28, v192
	v_cndmask_b32_e32 v208, v202, v192, vcc
	v_ashrrev_i32_e32 v209, 31, v208
	v_cndmask_b32_e32 v183, v161, v201, vcc
	v_cndmask_b32_e32 v182, v160, v200, vcc
	v_lshlrev_b64 v[208:209], 7, v[208:209]
	v_lshl_add_u64 v[182:183], v[182:183], 0, v[208:209]
	s_add_i32 s40, s6, s68
	v_lshl_add_u64 v[210:211], v[182:183], 0, v[186:187]
	s_mov_b32 m0, s40
	ds_read_b128 v[166:169], v225 offset:16384
	ds_read_b128 v[170:173], v225 offset:17408
	ds_read_b128 v[174:177], v225 offset:18432
	ds_read_b128 v[178:181], v225 offset:19456
	ds_read_b128 v[226:229], v225 offset:20480
	ds_read_b128 v[230:233], v225 offset:21504
	ds_read_b128 v[238:241], v225 offset:22528
	ds_read_b128 v[242:245], v225 offset:23552
	global_load_lds_dwordx4 v[210:211], off
	v_lshl_add_u64 v[210:211], v[182:183], 0, v[190:191]
	s_add_i32 m0, s40, 0x2000
	v_lshl_add_u64 v[182:183], v[182:183], 0, s[0:1]
	s_add_i32 s40, s79, s68
	global_load_lds_dwordx4 v[210:211], off
	v_lshl_add_u64 v[210:211], v[182:183], 0, v[186:187]
	s_mov_b32 m0, s40
	v_lshl_add_u64 v[182:183], v[182:183], 0, v[190:191]
	global_load_lds_dwordx4 v[210:211], off
	s_add_i32 m0, s40, 0x2000
	s_and_b64 s[40:41], vcc, exec
	s_cselect_b32 s41, s27, s29
	s_cselect_b32 s40, s26, s28
	global_load_lds_dwordx4 v[182:183], off
	v_lshl_add_u64 v[182:183], s[40:41], 0, v[208:209]
	v_lshl_add_u64 v[208:209], v[182:183], 0, v[184:185]
	s_mov_b32 m0, s70
	s_nop 0
	global_load_lds_dwordx4 v[208:209], off
	v_lshl_add_u64 v[208:209], v[182:183], 0, v[188:189]
	s_mov_b32 m0, s71
	s_nop 0
	global_load_lds_dwordx4 v[208:209], off
	s_waitcnt vmcnt(8)
	s_waitcnt lgkmcnt(0)
	s_barrier
	s_setprio 1
	s_waitcnt lgkmcnt(0)
	v_mfma_f32_16x16x128_f8f6f4 v[92:95], v[24:31], v[166:173], v[92:95]
	v_mfma_f32_16x16x128_f8f6f4 v[88:91], v[16:23], v[166:173], v[88:91]
	v_mfma_f32_16x16x128_f8f6f4 v[76:79], v[24:31], v[174:181], v[76:79]
	v_mfma_f32_16x16x128_f8f6f4 v[72:75], v[16:23], v[174:181], v[72:75]
	v_mfma_f32_16x16x128_f8f6f4 v[52:55], v[24:31], v[226:233], v[52:55]
	v_mfma_f32_16x16x128_f8f6f4 v[48:51], v[16:23], v[226:233], v[48:51]
	v_mfma_f32_16x16x128_f8f6f4 v[36:39], v[24:31], v[238:245], v[36:39]
	v_mfma_f32_16x16x128_f8f6f4 v[32:35], v[16:23], v[238:245], v[32:35]
	s_setprio 0
	s_setprio 1
	v_mfma_f32_16x16x128_f8f6f4 v[84:87], v[8:15], v[166:173], v[84:87]
	v_mfma_f32_16x16x128_f8f6f4 v[80:83], v[0:7], v[166:173], v[80:83]
	v_mfma_f32_16x16x128_f8f6f4 v[60:63], v[8:15], v[174:181], v[60:63]
	v_mfma_f32_16x16x128_f8f6f4 v[56:59], v[0:7], v[174:181], v[56:59]
	v_mfma_f32_16x16x128_f8f6f4 v[68:71], v[8:15], v[226:233], v[68:71]
	v_mfma_f32_16x16x128_f8f6f4 v[64:67], v[0:7], v[226:233], v[64:67]
	v_mfma_f32_16x16x128_f8f6f4 v[44:47], v[8:15], v[238:245], v[44:47]
	v_mfma_f32_16x16x128_f8f6f4 v[40:43], v[0:7], v[238:245], v[40:43]
	s_setprio 0
	s_barrier
	s_add_i32 s42, 0, 0x18000
	s_add_i32 s43, 0, 0x1c000
	v_add_u32_e32 v0, s42, v207
	v_add_u32_e32 v4, s43, v207
	ds_read_b128 v[16:19], v0
	ds_read_b128 v[20:23], v0 offset:1024
	ds_read_b128 v[24:27], v0 offset:2048
	ds_read_b128 v[28:31], v0 offset:3072
	ds_read_b128 v[8:11], v4
	ds_read_b128 v[12:15], v4 offset:1024
	ds_read_b128 v[0:3], v4 offset:2048
	ds_read_b128 v[4:7], v4 offset:3072
	v_lshl_add_u64 v[182:183], v[182:183], 0, s[0:1]
	s_mov_b32 m0, s77
	v_lshl_add_u64 v[208:209], v[182:183], 0, v[184:185]
	ds_read_b128 v[166:169], v225 offset:32768
	ds_read_b128 v[170:173], v225 offset:33792
	ds_read_b128 v[174:177], v225 offset:34816
	ds_read_b128 v[178:181], v225 offset:35840
	ds_read_b128 v[226:229], v225 offset:36864
	ds_read_b128 v[230:233], v225 offset:37888
	ds_read_b128 v[238:241], v225 offset:38912
	ds_read_b128 v[242:245], v225 offset:39936
	global_load_lds_dwordx4 v[208:209], off
	v_lshl_add_u64 v[182:183], v[182:183], 0, v[188:189]
	s_mov_b32 m0, s78
	s_nop 0
	global_load_lds_dwordx4 v[182:183], off
	s_waitcnt vmcnt(8)
	s_waitcnt lgkmcnt(0)
	s_barrier
	s_setprio 1
	s_waitcnt lgkmcnt(0)
	v_mfma_f32_16x16x128_f8f6f4 v[156:159], v[16:23], v[166:173], v[156:159]
	v_mfma_f32_16x16x128_f8f6f4 v[152:155], v[24:31], v[166:173], v[152:155]
	v_mfma_f32_16x16x128_f8f6f4 v[140:143], v[16:23], v[174:181], v[140:143]
	v_mfma_f32_16x16x128_f8f6f4 v[136:139], v[24:31], v[174:181], v[136:139]
	v_mfma_f32_16x16x128_f8f6f4 v[124:127], v[16:23], v[226:233], v[124:127]
	v_mfma_f32_16x16x128_f8f6f4 v[120:123], v[24:31], v[226:233], v[120:123]
	v_mfma_f32_16x16x128_f8f6f4 v[108:111], v[16:23], v[238:245], v[108:111]
	v_mfma_f32_16x16x128_f8f6f4 v[104:107], v[24:31], v[238:245], v[104:107]
	s_setprio 0
	s_setprio 1
	v_mfma_f32_16x16x128_f8f6f4 v[148:151], v[8:15], v[166:173], v[148:151]
	v_mfma_f32_16x16x128_f8f6f4 v[144:147], v[0:7], v[166:173], v[144:147]
	v_mfma_f32_16x16x128_f8f6f4 v[132:135], v[8:15], v[174:181], v[132:135]
	v_mfma_f32_16x16x128_f8f6f4 v[128:131], v[0:7], v[174:181], v[128:131]
	v_mfma_f32_16x16x128_f8f6f4 v[116:119], v[8:15], v[226:233], v[116:119]
	v_mfma_f32_16x16x128_f8f6f4 v[112:115], v[0:7], v[226:233], v[112:115]
	v_mfma_f32_16x16x128_f8f6f4 v[100:103], v[8:15], v[238:245], v[100:103]
	v_mfma_f32_16x16x128_f8f6f4 v[96:99], v[0:7], v[238:245], v[96:99]
	s_setprio 0
	s_barrier
	s_cmp_gt_u32 s39, 24
	s_cselect_b64 vcc, -1, 0
	s_and_b64 s[40:41], vcc, exec
	s_cselect_b32 s40, 0xffffffe7, 3
	s_add_i32 s40, s40, s39
	s_ashr_i32 s41, s40, 31
	v_cndmask_b32_e32 v183, v161, v201, vcc
	v_cndmask_b32_e32 v182, v160, v200, vcc
	s_lshl_b64 s[40:41], s[40:41], 7
	v_lshl_add_u64 v[182:183], v[182:183], 0, s[40:41]
	s_add_i32 s42, s42, s68
	v_lshl_add_u64 v[208:209], v[182:183], 0, v[186:187]
	s_mov_b32 m0, s42
	ds_read_b128 v[166:169], v225 offset:49152
	ds_read_b128 v[170:173], v225 offset:50176
	ds_read_b128 v[174:177], v225 offset:51200
	ds_read_b128 v[178:181], v225 offset:52224
	ds_read_b128 v[226:229], v225 offset:53248
	ds_read_b128 v[230:233], v225 offset:54272
	ds_read_b128 v[238:241], v225 offset:55296
	ds_read_b128 v[242:245], v225 offset:56320
	global_load_lds_dwordx4 v[208:209], off
	v_lshl_add_u64 v[208:209], v[182:183], 0, v[190:191]
	s_add_i32 m0, s42, 0x2000
	v_lshl_add_u64 v[182:183], v[182:183], 0, s[0:1]
	s_add_i32 s42, s43, s68
	global_load_lds_dwordx4 v[208:209], off
	v_lshl_add_u64 v[208:209], v[182:183], 0, v[186:187]
	s_mov_b32 m0, s42
	v_lshl_add_u64 v[182:183], v[182:183], 0, v[190:191]
	global_load_lds_dwordx4 v[208:209], off
	s_add_i32 m0, s42, 0x2000
	s_and_b64 s[42:43], vcc, exec
	s_cselect_b32 s43, s26, s28
	s_cselect_b32 s42, s27, s29
	s_add_u32 s40, s43, s40
	s_addc_u32 s41, s42, s41
	global_load_lds_dwordx4 v[182:183], off
	v_lshl_add_u64 v[182:183], s[40:41], 0, v[184:185]
	s_mov_b32 m0, s54
	s_nop 0
	global_load_lds_dwordx4 v[182:183], off
	v_lshl_add_u64 v[182:183], s[40:41], 0, v[188:189]
	s_mov_b32 m0, s55
	s_nop 0
	global_load_lds_dwordx4 v[182:183], off
	s_waitcnt vmcnt(8)
	s_waitcnt lgkmcnt(0)
	s_barrier
	s_setprio 1
	s_waitcnt lgkmcnt(0)
	v_mfma_f32_16x16x128_f8f6f4 v[92:95], v[16:23], v[166:173], v[92:95]
	v_mfma_f32_16x16x128_f8f6f4 v[88:91], v[24:31], v[166:173], v[88:91]
	v_mfma_f32_16x16x128_f8f6f4 v[76:79], v[16:23], v[174:181], v[76:79]
	v_mfma_f32_16x16x128_f8f6f4 v[72:75], v[24:31], v[174:181], v[72:75]
	v_mfma_f32_16x16x128_f8f6f4 v[52:55], v[16:23], v[226:233], v[52:55]
	v_mfma_f32_16x16x128_f8f6f4 v[48:51], v[24:31], v[226:233], v[48:51]
	v_mfma_f32_16x16x128_f8f6f4 v[36:39], v[16:23], v[238:245], v[36:39]
	v_mfma_f32_16x16x128_f8f6f4 v[32:35], v[24:31], v[238:245], v[32:35]
	s_setprio 0
	s_setprio 1
	v_mfma_f32_16x16x128_f8f6f4 v[84:87], v[8:15], v[166:173], v[84:87]
	v_mfma_f32_16x16x128_f8f6f4 v[80:83], v[0:7], v[166:173], v[80:83]
	v_mfma_f32_16x16x128_f8f6f4 v[60:63], v[8:15], v[174:181], v[60:63]
	v_mfma_f32_16x16x128_f8f6f4 v[56:59], v[0:7], v[174:181], v[56:59]
	v_mfma_f32_16x16x128_f8f6f4 v[68:71], v[8:15], v[226:233], v[68:71]
	v_mfma_f32_16x16x128_f8f6f4 v[64:67], v[0:7], v[226:233], v[64:67]
	v_mfma_f32_16x16x128_f8f6f4 v[44:47], v[8:15], v[238:245], v[44:47]
	v_mfma_f32_16x16x128_f8f6f4 v[40:43], v[0:7], v[238:245], v[40:43]
	s_setprio 0
	s_barrier
	v_lshl_add_u64 v[162:163], v[162:163], 0, s[24:25]
	v_lshl_add_u64 v[164:165], v[164:165], 0, s[24:25]
	s_add_i32 s39, s39, 2
	s_and_b64 vcc, exec, s[30:31]
	s_cbranch_vccnz .LBB0_1373
	s_andn2_b64 vcc, exec, s[22:23]
	s_cbranch_vccnz .LBB0_1376
	s_barrier

	.amdhsa_kernel _Z10fwd_kernel4Args
		.amdhsa_group_segment_fixed_size 0
		.amdhsa_private_segment_fixed_size 0
		.amdhsa_kernarg_size 456
		.amdhsa_user_sgpr_count 2
		.amdhsa_user_sgpr_dispatch_ptr 0
		.amdhsa_user_sgpr_queue_ptr 0
		.amdhsa_user_sgpr_kernarg_segment_ptr 1
		.amdhsa_user_sgpr_dispatch_id 0
		.amdhsa_user_sgpr_kernarg_preload_length 0
		.amdhsa_user_sgpr_kernarg_preload_offset 0
		.amdhsa_user_sgpr_private_segment_size 0
		.amdhsa_uses_dynamic_stack 0
		.amdhsa_enable_private_segment 0
		.amdhsa_system_sgpr_workgroup_id_x 1
		.amdhsa_system_sgpr_workgroup_id_y 0
		.amdhsa_system_sgpr_workgroup_id_z 0
		.amdhsa_system_sgpr_workgroup_info 0
		.amdhsa_system_vgpr_workitem_id 0
		.amdhsa_next_free_vgpr 256
		.amdhsa_next_free_sgpr 102
		.amdhsa_accum_offset 256
		.amdhsa_reserve_vcc 1
		.amdhsa_float_round_mode_32 0
		.amdhsa_float_round_mode_16_64 0
		.amdhsa_float_denorm_mode_32 3
		.amdhsa_float_denorm_mode_16_64 3
		.amdhsa_dx10_clamp 1
		.amdhsa_ieee_mode 1
		.amdhsa_fp16_overflow 0
		.amdhsa_tg_split 0
		.amdhsa_exception_fp_ieee_invalid_op 0
		.amdhsa_exception_fp_denorm_src 0
		.amdhsa_exception_fp_ieee_div_zero 0
		.amdhsa_exception_fp_ieee_overflow 0
		.amdhsa_exception_fp_ieee_underflow 0
		.amdhsa_exception_fp_ieee_inexact 0
		.amdhsa_exception_int_div_zero 0
	.end_amdhsa_kernel

amdhsa.kernels:
  - .agpr_count:     0
    .args:
      - .offset:         0
        .size:           200
        .value_kind:     by_value
      - .offset:         200
        .size:           4
        .value_kind:     hidden_block_count_x
      - .offset:         204
        .size:           4
        .value_kind:     hidden_block_count_y
      - .offset:         208
        .size:           4
        .value_kind:     hidden_block_count_z
      - .offset:         212
        .size:           2
        .value_kind:     hidden_group_size_x
      - .offset:         214
        .size:           2
        .value_kind:     hidden_group_size_y
      - .offset:         216
        .size:           2
        .value_kind:     hidden_group_size_z
      - .offset:         218
        .size:           2
        .value_kind:     hidden_remainder_x
      - .offset:         220
        .size:           2
        .value_kind:     hidden_remainder_y
      - .offset:         222
        .size:           2
        .value_kind:     hidden_remainder_z
      - .offset:         240
        .size:           8
        .value_kind:     hidden_global_offset_x
      - .offset:         248
        .size:           8
        .value_kind:     hidden_global_offset_y
      - .offset:         256
        .size:           8
        .value_kind:     hidden_global_offset_z
      - .offset:         264
        .size:           2
        .value_kind:     hidden_grid_dims
      - .offset:         320
        .size:           4
        .value_kind:     hidden_dynamic_lds_size
    .group_segment_fixed_size: 0
    .kernarg_segment_align: 8
    .kernarg_segment_size: 456
    .language:       OpenCL C
    .language_version:
      - 2
      - 0
    .max_flat_workgroup_size: 512
    .name:           _Z10fwd_kernel4Args
    .private_segment_fixed_size: 0
    .sgpr_count:     108
    .sgpr_spill_count: 115
    .symbol:         _Z10fwd_kernel4Args.kd
    .uniform_work_group_size: 1
    .uses_dynamic_stack: false
    .vgpr_count:     256
    .vgpr_spill_count: 0
    .wavefront_size: 64
